# speedup vs baseline: 1.0194x; 1.0194x over previous
_Z16bilateral_kernelPKfS0_Pf:
	s_load_dwordx2 s[4:5], s[0:1], 0x0
	s_load_dwordx2 s[8:9], s[0:1], 0x10
	s_and_b32 s0, s2, 7
	s_mulk_i32 s0, 0x60
	s_lshr_b32 s1, s2, 3
	s_add_i32 s1, s0, s1
	s_lshr_b32 s0, s1, 6
	s_lshl_b32 s11, s1, 6
	s_and_b32 s11, s11, 0x1c0
	s_lshl_b32 s1, s1, 3
	s_nop 0
	s_and_b32 s10, s1, 0x1c0
	s_mov_b32 s1, 0
	s_lshl_b64 s[2:3], s[0:1], 20
	s_mov_b32 s20, 0xc05dfbe6
	s_mov_b32 s21, 0xc05dfbe6
	s_mov_b32 s22, 0xc0a8390e
	s_mov_b32 s23, 0xc0a8390e
	s_mov_b32 s24, 0xc08211a7
	s_mov_b32 s25, 0xc08211a7
	s_mov_b32 s26, 0xc0bb4cc1
	s_mov_b32 s27, 0xc0bb4cc1
	s_mov_b32 s28, 0xc0f487dc
	s_mov_b32 s29, 0xc0f487dc
	s_mov_b32 s30, 0x3e0bd796
	s_mov_b32 s31, 0x3e0bd796
	s_mov_b32 s32, 0x3f45a90c
	s_mov_b32 s33, 0x3f45a90c
	s_mov_b32 s34, 0x3fa5c782
	s_mov_b32 s35, 0x3fa5c782
	v_and_b32_e32 v118, 15, v0
	v_lshrrev_b32_e32 v115, 2, v0
	v_lshl_or_b32 v113, v118, 2, s11
	v_and_or_b32 v117, v115, 60, s10
	v_min_u32_e32 v116, 0x1fa, v113
	v_sub_u32_e64 v115, v113, 2 clamp
	v_add_u32_e64 v116, 4, v116
	v_cmp_eq_u32_e64 s[16:17], 0, v118
	v_cmp_eq_u32_e32 vcc, 15, v118
	s_nop 1
	v_cndmask_b32_e64 v115, v116, v115, s[16:17]
	s_or_b64 vcc, s[16:17], vcc
	v_lshlrev_b32_e32 v115, 2, v115
	v_mov_b32_e32 v116, 0x7ff00000
	s_nop 0
	v_cndmask_b32_e32 v112, v116, v115, vcc
	s_movk_i32 s18, 0x1fc
	v_cmp_eq_u32_e32 vcc, 0, v113
	v_cmp_eq_u32_e64 s[16:17], s18, v113
	v_lshlrev_b32_e32 v113, 2, v113
	s_waitcnt lgkmcnt(0)
	s_add_u32 s4, s4, s2
	s_addc_u32 s5, s5, s3
	s_and_b32 s5, s5, 0xffff
	s_mov_b32 s6, 0x100000
	s_mov_b32 s7, 0x20000
	s_add_u32 s12, s8, s2
	s_addc_u32 s13, s9, s3
	s_and_b32 s13, s13, 0xffff
	s_mov_b32 s14, 0x100000
	s_mov_b32 s15, 0x20000
	v_sub_u32_e64 v115, v117, 2 clamp
	v_lshlrev_b32_e32 v115, 11, v115
	v_add_u32_e32 v116, v115, v112
	v_add_u32_e64 v115, v115, v113
	buffer_load_dwordx2 v[0:1], v116, s[4:7], 0 offen nt
	buffer_load_dwordx2 v[6:7], v116, s[4:7], 0 offen nt
	buffer_load_dwordx4 v[2:5], v115, s[4:7], 0 offen nt
	v_sub_u32_e64 v115, v117, 1 clamp
	v_lshlrev_b32_e32 v115, 11, v115
	v_add_u32_e32 v116, v115, v112
	v_add_u32_e64 v115, v115, v113
	buffer_load_dwordx2 v[8:9], v116, s[4:7], 0 offen nt
	buffer_load_dwordx2 v[14:15], v116, s[4:7], 0 offen nt
	buffer_load_dwordx4 v[10:13], v115, s[4:7], 0 offen nt
	v_lshlrev_b32_e32 v115, 11, v117
	v_add_u32_e32 v116, v115, v112
	v_add_u32_e64 v114, v115, v113
	v_add_u32_e32 v119, 0x1000, v114
	buffer_load_dwordx2 v[16:17], v116, s[4:7], 0 offen nt
	buffer_load_dwordx2 v[22:23], v116, s[4:7], 0 offen nt
	buffer_load_dwordx4 v[18:21], v114, s[4:7], 0 offen nt
	v_lshlrev_b32_e64 v115, 11, v117
	v_add_u32_e32 v115, 0x800, v115
	v_add_u32_e32 v116, v115, v112
	v_add_u32_e32 v115, v115, v113
	buffer_load_dwordx2 v[24:25], v116, s[4:7], 0 offen nt
	buffer_load_dwordx2 v[30:31], v116, s[4:7], 0 offen nt
	buffer_load_dwordx4 v[26:29], v115, s[4:7], 0 offen nt
	v_lshlrev_b32_e64 v115, 11, v117
	v_add_u32_e32 v115, 0x1000, v115
	v_add_u32_e32 v116, v115, v112
	v_add_u32_e32 v115, v115, v113
	buffer_load_dwordx2 v[32:33], v116, s[4:7], 0 offen nt
	buffer_load_dwordx2 v[38:39], v116, s[4:7], 0 offen nt
	buffer_load_dwordx4 v[34:37], v115, s[4:7], 0 offen nt
	v_lshlrev_b32_e64 v115, 11, v117
	v_add_u32_e32 v115, 0x1800, v115
	v_add_u32_e32 v116, v115, v112
	v_add_u32_e32 v115, v115, v113
	buffer_load_dwordx2 v[40:41], v116, s[4:7], 0 offen nt
	buffer_load_dwordx2 v[46:47], v116, s[4:7], 0 offen nt
	buffer_load_dwordx4 v[42:45], v115, s[4:7], 0 offen nt
	v_min_u32_e32 v115, 0x1fb, v117
	v_lshlrev_b32_e64 v115, 11, v115
	v_add_u32_e32 v115, 0x2000, v115
	v_add_u32_e32 v116, v115, v112
	v_add_u32_e32 v115, v115, v113
	buffer_load_dwordx2 v[48:49], v116, s[4:7], 0 offen nt
	buffer_load_dwordx2 v[54:55], v116, s[4:7], 0 offen nt
	buffer_load_dwordx4 v[50:53], v115, s[4:7], 0 offen nt
	v_min_u32_e32 v115, 0x1fa, v117
	v_lshlrev_b32_e64 v115, 11, v115
	v_add_u32_e32 v115, 0x2800, v115
	v_add_u32_e32 v116, v115, v112
	v_add_u32_e32 v115, v115, v113
	buffer_load_dwordx2 v[56:57], v116, s[4:7], 0 offen nt
	buffer_load_dwordx2 v[62:63], v116, s[4:7], 0 offen nt
	buffer_load_dwordx4 v[58:61], v115, s[4:7], 0 offen nt
	s_waitcnt vmcnt(21)
	s_nop 0
	v_mov_b32_dpp v0, v4 row_shr:1 row_mask:0xf bank_mask:0xf
	v_mov_b32_dpp v1, v5 row_shr:1 row_mask:0xf bank_mask:0xf
	v_mov_b32_dpp v6, v2 row_shl:1 row_mask:0xf bank_mask:0xf
	v_mov_b32_dpp v7, v3 row_shl:1 row_mask:0xf bank_mask:0xf
	v_pk_mul_f32 v[2:3], v[2:3], s[32:33]
	v_pk_mul_f32 v[4:5], v[4:5], s[32:33]
	v_cndmask_b32_e64 v1, v1, v0, vcc
	v_cndmask_b32_e64 v6, v6, v7, s[16:17]
	v_pk_mul_f32 v[0:1], v[0:1], s[32:33]
	v_pk_mul_f32 v[6:7], v[6:7], s[32:33]
	s_waitcnt vmcnt(18)
	s_nop 0
	v_mov_b32_dpp v8, v12 row_shr:1 row_mask:0xf bank_mask:0xf
	v_mov_b32_dpp v9, v13 row_shr:1 row_mask:0xf bank_mask:0xf
	v_mov_b32_dpp v14, v10 row_shl:1 row_mask:0xf bank_mask:0xf
	v_mov_b32_dpp v15, v11 row_shl:1 row_mask:0xf bank_mask:0xf
	v_pk_mul_f32 v[10:11], v[10:11], s[32:33]
	v_pk_mul_f32 v[12:13], v[12:13], s[32:33]
	v_cndmask_b32_e64 v9, v9, v8, vcc
	v_cndmask_b32_e64 v14, v14, v15, s[16:17]
	v_pk_mul_f32 v[8:9], v[8:9], s[32:33]
	v_pk_mul_f32 v[14:15], v[14:15], s[32:33]
	s_waitcnt vmcnt(15)
	s_nop 0
	v_mov_b32_dpp v16, v20 row_shr:1 row_mask:0xf bank_mask:0xf
	v_mov_b32_dpp v17, v21 row_shr:1 row_mask:0xf bank_mask:0xf
	v_mov_b32_dpp v22, v18 row_shl:1 row_mask:0xf bank_mask:0xf
	v_mov_b32_dpp v23, v19 row_shl:1 row_mask:0xf bank_mask:0xf
	v_pk_mul_f32 v[18:19], v[18:19], s[32:33]
	v_pk_mul_f32 v[20:21], v[20:21], s[32:33]
	v_cndmask_b32_e64 v17, v17, v16, vcc
	v_cndmask_b32_e64 v22, v22, v23, s[16:17]
	v_pk_mul_f32 v[68:69], v[18:19], s[30:31]
	v_pk_mul_f32 v[70:71], v[20:21], s[30:31]
	v_pk_mul_f32 v[16:17], v[16:17], s[32:33]
	v_pk_mul_f32 v[22:23], v[22:23], s[32:33]
	s_setprio 3
	s_nop 0
	v_pk_add_f32 v[96:97], v[18:19], v[0:1] neg_lo:[0,1] neg_hi:[0,1]
	v_pk_add_f32 v[98:99], v[18:19], v[2:3] neg_lo:[0,1] neg_hi:[0,1]
	v_pk_add_f32 v[100:101], v[20:21], v[2:3] neg_lo:[0,1] neg_hi:[0,1]
	v_pk_add_f32 v[102:103], v[18:19], v[4:5] neg_lo:[0,1] neg_hi:[0,1]
	v_pk_fma_f32 v[96:97], v[96:97], v[96:97], s[28:29] neg_lo:[1,0,0] neg_hi:[1,0,0]
	v_pk_fma_f32 v[98:99], v[98:99], v[98:99], s[22:23] neg_lo:[1,0,0] neg_hi:[1,0,0]
	v_pk_fma_f32 v[100:101], v[100:101], v[100:101], s[28:29] neg_lo:[1,0,0] neg_hi:[1,0,0]
	v_pk_fma_f32 v[102:103], v[102:103], v[102:103], s[28:29] neg_lo:[1,0,0] neg_hi:[1,0,0]
	v_exp_f32_e32 v96, v96
	v_exp_f32_e32 v97, v97
	v_exp_f32_e32 v98, v98
	v_exp_f32_e32 v99, v99
	v_exp_f32_e32 v100, v100
	v_exp_f32_e32 v101, v101
	v_exp_f32_e32 v102, v102
	v_exp_f32_e32 v103, v103
	v_pk_add_f32 v[104:105], v[20:21], v[4:5] neg_lo:[0,1] neg_hi:[0,1]
	v_pk_add_f32 v[106:107], v[20:21], v[6:7] neg_lo:[0,1] neg_hi:[0,1]
	v_pk_add_f32 v[108:109], v[18:19], v[2:3] op_sel:[1,0] op_sel_hi:[0,1] neg_lo:[0,1] neg_hi:[0,1]
	v_pk_add_f32 v[110:111], v[20:21], v[4:5] op_sel:[1,0] op_sel_hi:[0,1] neg_lo:[0,1] neg_hi:[0,1]
	v_pk_fma_f32 v[104:105], v[104:105], v[104:105], s[22:23] neg_lo:[1,0,0] neg_hi:[1,0,0]
	v_pk_fma_f32 v[106:107], v[106:107], v[106:107], s[28:29] neg_lo:[1,0,0] neg_hi:[1,0,0]
	v_pk_fma_f32 v[108:109], v[108:109], v[108:109], s[26:27] neg_lo:[1,0,0] neg_hi:[1,0,0]
	v_pk_fma_f32 v[110:111], v[110:111], v[110:111], s[26:27] neg_lo:[1,0,0] neg_hi:[1,0,0]
	v_exp_f32_e32 v104, v104
	v_exp_f32_e32 v105, v105
	v_exp_f32_e32 v106, v106
	v_exp_f32_e32 v107, v107
	v_exp_f32_e32 v108, v108
	v_exp_f32_e32 v109, v109
	v_exp_f32_e32 v110, v110
	v_exp_f32_e32 v111, v111
	v_pk_add_f32 v[64:65], s[30:31], v[96:97]
	v_pk_fma_f32 v[68:69], v[96:97], v[0:1], v[68:69]
	v_pk_add_f32 v[66:67], s[30:31], v[100:101]
	v_pk_add_f32 v[64:65], v[64:65], v[98:99]
	v_pk_fma_f32 v[68:69], v[98:99], v[2:3], v[68:69]
	v_pk_fma_f32 v[70:71], v[100:101], v[2:3], v[70:71]
	v_pk_add_f32 v[64:65], v[64:65], v[102:103]
	v_pk_fma_f32 v[68:69], v[102:103], v[4:5], v[68:69]
	v_pk_add_f32 v[96:97], v[18:19], v[8:9] neg_lo:[0,1] neg_hi:[0,1]
	v_pk_add_f32 v[98:99], v[18:19], v[10:11] neg_lo:[0,1] neg_hi:[0,1]
	v_pk_add_f32 v[100:101], v[20:21], v[10:11] neg_lo:[0,1] neg_hi:[0,1]
	v_pk_add_f32 v[102:103], v[18:19], v[12:13] neg_lo:[0,1] neg_hi:[0,1]
	v_pk_fma_f32 v[96:97], v[96:97], v[96:97], s[26:27] neg_lo:[1,0,0] neg_hi:[1,0,0]
	v_pk_fma_f32 v[98:99], v[98:99], v[98:99], s[20:21] neg_lo:[1,0,0] neg_hi:[1,0,0]
	v_pk_fma_f32 v[100:101], v[100:101], v[100:101], s[26:27] neg_lo:[1,0,0] neg_hi:[1,0,0]
	v_pk_fma_f32 v[102:103], v[102:103], v[102:103], s[26:27] neg_lo:[1,0,0] neg_hi:[1,0,0]
	v_exp_f32_e32 v96, v96
	v_exp_f32_e32 v97, v97
	v_exp_f32_e32 v98, v98
	v_exp_f32_e32 v99, v99
	v_exp_f32_e32 v100, v100
	v_exp_f32_e32 v101, v101
	v_exp_f32_e32 v102, v102
	v_exp_f32_e32 v103, v103
	v_pk_add_f32 v[66:67], v[66:67], v[104:105]
	v_pk_fma_f32 v[70:71], v[104:105], v[4:5], v[70:71]
	v_pk_add_f32 v[64:65], v[64:65], v[108:109] op_sel:[0,1] op_sel_hi:[1,0]
	v_pk_add_f32 v[66:67], v[66:67], v[106:107]
	v_pk_fma_f32 v[70:71], v[106:107], v[6:7], v[70:71]
	v_pk_fma_f32 v[68:69], v[108:109], v[2:3], v[68:69] op_sel:[1,1,0] op_sel_hi:[0,0,1]
	v_pk_add_f32 v[66:67], v[66:67], v[110:111] op_sel:[0,1] op_sel_hi:[1,0]
	v_pk_fma_f32 v[70:71], v[110:111], v[4:5], v[70:71] op_sel:[1,1,0] op_sel_hi:[0,0,1]
	v_pk_add_f32 v[104:105], v[20:21], v[12:13] neg_lo:[0,1] neg_hi:[0,1]
	v_pk_add_f32 v[106:107], v[20:21], v[14:15] neg_lo:[0,1] neg_hi:[0,1]
	v_pk_add_f32 v[108:109], v[18:19], v[10:11] op_sel:[1,0] op_sel_hi:[0,1] neg_lo:[0,1] neg_hi:[0,1]
	v_pk_add_f32 v[110:111], v[20:21], v[12:13] op_sel:[1,0] op_sel_hi:[0,1] neg_lo:[0,1] neg_hi:[0,1]
	v_pk_fma_f32 v[104:105], v[104:105], v[104:105], s[20:21] neg_lo:[1,0,0] neg_hi:[1,0,0]
	v_pk_fma_f32 v[106:107], v[106:107], v[106:107], s[26:27] neg_lo:[1,0,0] neg_hi:[1,0,0]
	v_pk_fma_f32 v[108:109], v[108:109], v[108:109], s[24:25] neg_lo:[1,0,0] neg_hi:[1,0,0]
	v_pk_fma_f32 v[110:111], v[110:111], v[110:111], s[24:25] neg_lo:[1,0,0] neg_hi:[1,0,0]
	v_exp_f32_e32 v104, v104
	v_exp_f32_e32 v105, v105
	v_exp_f32_e32 v106, v106
	v_exp_f32_e32 v107, v107
	v_exp_f32_e32 v108, v108
	v_exp_f32_e32 v109, v109
	v_exp_f32_e32 v110, v110
	v_exp_f32_e32 v111, v111
	v_pk_add_f32 v[64:65], v[64:65], v[96:97]
	v_pk_fma_f32 v[68:69], v[96:97], v[8:9], v[68:69]
	v_pk_add_f32 v[66:67], v[66:67], v[100:101]
	v_pk_add_f32 v[64:65], v[64:65], v[98:99]
	v_pk_fma_f32 v[68:69], v[98:99], v[10:11], v[68:69]
	v_pk_fma_f32 v[70:71], v[100:101], v[10:11], v[70:71]
	v_pk_add_f32 v[64:65], v[64:65], v[102:103]
	v_pk_fma_f32 v[68:69], v[102:103], v[12:13], v[68:69]
	v_pk_add_f32 v[96:97], v[18:19], v[16:17] neg_lo:[0,1] neg_hi:[0,1]
	v_pk_add_f32 v[98:99], v[20:21], v[18:19] neg_lo:[0,1] neg_hi:[0,1]
	v_pk_add_f32 v[100:101], v[22:23], v[20:21] neg_lo:[0,1] neg_hi:[0,1]
	v_pk_fma_f32 v[96:97], v[96:97], v[96:97], s[22:23] neg_lo:[1,0,0] neg_hi:[1,0,0]
	v_pk_fma_f32 v[98:99], v[98:99], v[98:99], s[22:23] neg_lo:[1,0,0] neg_hi:[1,0,0]
	v_pk_fma_f32 v[100:101], v[100:101], v[100:101], s[22:23] neg_lo:[1,0,0] neg_hi:[1,0,0]
	v_exp_f32_e32 v96, v96
	v_exp_f32_e32 v97, v97
	v_exp_f32_e32 v98, v98
	v_exp_f32_e32 v99, v99
	v_exp_f32_e32 v100, v100
	v_exp_f32_e32 v101, v101
	v_pk_add_f32 v[66:67], v[66:67], v[104:105]
	v_pk_fma_f32 v[70:71], v[104:105], v[12:13], v[70:71]
	v_pk_add_f32 v[64:65], v[64:65], v[108:109] op_sel:[0,1] op_sel_hi:[1,0]
	v_pk_add_f32 v[66:67], v[66:67], v[106:107]
	v_pk_fma_f32 v[70:71], v[106:107], v[14:15], v[70:71]
	v_pk_fma_f32 v[68:69], v[108:109], v[10:11], v[68:69] op_sel:[1,1,0] op_sel_hi:[0,0,1]
	v_pk_add_f32 v[66:67], v[66:67], v[110:111] op_sel:[0,1] op_sel_hi:[1,0]
	v_pk_fma_f32 v[70:71], v[110:111], v[12:13], v[70:71] op_sel:[1,1,0] op_sel_hi:[0,0,1]
	v_sub_f32_e32 v104, v18, v1
	v_sub_f32_e32 v106, v20, v3
	v_sub_f32_e32 v108, v19, v4
	v_sub_f32_e32 v110, v21, v6
	v_sub_f32_e32 v105, v18, v9
	v_sub_f32_e32 v107, v20, v11
	v_sub_f32_e32 v109, v19, v12
	v_sub_f32_e32 v111, v21, v14
	v_fma_f32 v104, -v104, v104, s26
	v_fma_f32 v106, -v106, v106, s26
	v_fma_f32 v108, -v108, v108, s26
	v_fma_f32 v110, -v110, v110, s26
	v_fma_f32 v105, -v105, v105, s24
	v_fma_f32 v107, -v107, v107, s24
	v_fma_f32 v109, -v109, v109, s24
	v_fma_f32 v111, -v111, v111, s24
	v_exp_f32_e32 v104, v104
	v_exp_f32_e32 v106, v106
	v_exp_f32_e32 v108, v108
	v_exp_f32_e32 v110, v110
	v_exp_f32_e32 v105, v105
	v_exp_f32_e32 v107, v107
	v_exp_f32_e32 v109, v109
	v_exp_f32_e32 v111, v111
	v_pk_add_f32 v[64:65], v[64:65], v[96:97]
	v_pk_fma_f32 v[68:69], v[96:97], v[16:17], v[68:69]
	v_pk_add_f32 v[66:67], v[66:67], v[98:99]
	v_pk_add_f32 v[64:65], v[64:65], v[98:99]
	v_pk_fma_f32 v[68:69], v[98:99], v[20:21], v[68:69]
	v_pk_fma_f32 v[70:71], v[98:99], v[18:19], v[70:71]
	v_pk_add_f32 v[66:67], v[66:67], v[100:101]
	v_pk_fma_f32 v[70:71], v[100:101], v[22:23], v[70:71]
	v_sub_f32_e32 v100, v18, v17
	v_sub_f32_e32 v96, v19, v18
	v_sub_f32_e32 v102, v20, v19
	v_sub_f32_e32 v98, v21, v20
	v_sub_f32_e64 v97, v22, v21
	v_fma_f32 v100, -v100, v100, s20
	v_fma_f32 v96, -v96, v96, s20
	v_fma_f32 v102, -v102, v102, s20
	v_fma_f32 v98, -v98, v98, s20
	v_fma_f32 v97, -v97, v97, s20
	v_exp_f32_e32 v100, v100
	v_exp_f32_e32 v96, v96
	v_exp_f32_e32 v102, v102
	v_exp_f32_e32 v98, v98
	v_exp_f32_e32 v97, v97
	v_add_f32_e32 v64, v64, v104
	v_fmac_f32_e32 v68, v104, v1
	v_add_f32_e32 v66, v66, v106
	v_fmac_f32_e32 v70, v106, v3
	v_add_f32_e32 v65, v65, v108
	v_fmac_f32_e32 v69, v108, v4
	v_add_f32_e32 v67, v67, v110
	v_fmac_f32_e32 v71, v110, v6
	v_add_f32_e32 v64, v64, v105
	v_fmac_f32_e32 v68, v105, v9
	v_add_f32_e32 v66, v66, v107
	v_fmac_f32_e32 v70, v107, v11
	v_add_f32_e32 v65, v65, v109
	v_fmac_f32_e32 v69, v109, v12
	v_add_f32_e32 v67, v67, v111
	v_fmac_f32_e32 v71, v111, v14
	v_add_f32_e32 v64, v64, v100
	v_fmac_f32_e32 v68, v100, v17
	v_add_f32_e32 v65, v65, v102
	v_fmac_f32_e32 v69, v102, v20
	v_add_f32_e32 v66, v66, v102
	v_fmac_f32_e32 v70, v102, v19
	v_add_f32_e32 v67, v67, v97
	v_fmac_f32_e64 v71, v97, v22
	v_pk_add_f32 v[64:65], v[64:65], v[96:97] op_sel_hi:[1,0]
	v_pk_fma_f32 v[68:69], v[96:97], v[18:19], v[68:69] op_sel:[0,1,0] op_sel_hi:[0,0,1]
	v_pk_add_f32 v[66:67], v[66:67], v[98:99] op_sel_hi:[1,0]
	v_pk_fma_f32 v[70:71], v[98:99], v[20:21], v[70:71] op_sel:[0,1,0] op_sel_hi:[0,0,1]
	s_waitcnt vmcnt(12)
	s_nop 0
	v_mov_b32_dpp v24, v28 row_shr:1 row_mask:0xf bank_mask:0xf
	v_mov_b32_dpp v25, v29 row_shr:1 row_mask:0xf bank_mask:0xf
	v_mov_b32_dpp v30, v26 row_shl:1 row_mask:0xf bank_mask:0xf
	v_mov_b32_dpp v31, v27 row_shl:1 row_mask:0xf bank_mask:0xf
	v_pk_mul_f32 v[26:27], v[26:27], s[32:33]
	v_pk_mul_f32 v[28:29], v[28:29], s[32:33]
	v_cndmask_b32_e64 v25, v25, v24, vcc
	v_cndmask_b32_e64 v30, v30, v31, s[16:17]
	v_pk_mul_f32 v[76:77], v[26:27], s[30:31]
	v_pk_mul_f32 v[78:79], v[28:29], s[30:31]
	v_pk_mul_f32 v[24:25], v[24:25], s[32:33]
	v_pk_mul_f32 v[30:31], v[30:31], s[32:33]
	s_setprio 3
	s_nop 0
	v_pk_add_f32 v[96:97], v[26:27], v[8:9] neg_lo:[0,1] neg_hi:[0,1]
	v_pk_add_f32 v[98:99], v[26:27], v[10:11] neg_lo:[0,1] neg_hi:[0,1]
	v_pk_add_f32 v[100:101], v[28:29], v[10:11] neg_lo:[0,1] neg_hi:[0,1]
	v_pk_add_f32 v[102:103], v[26:27], v[12:13] neg_lo:[0,1] neg_hi:[0,1]
	v_pk_fma_f32 v[96:97], v[96:97], v[96:97], s[28:29] neg_lo:[1,0,0] neg_hi:[1,0,0]
	v_pk_fma_f32 v[98:99], v[98:99], v[98:99], s[22:23] neg_lo:[1,0,0] neg_hi:[1,0,0]
	v_pk_fma_f32 v[100:101], v[100:101], v[100:101], s[28:29] neg_lo:[1,0,0] neg_hi:[1,0,0]
	v_pk_fma_f32 v[102:103], v[102:103], v[102:103], s[28:29] neg_lo:[1,0,0] neg_hi:[1,0,0]
	v_exp_f32_e32 v96, v96
	v_exp_f32_e32 v97, v97
	v_exp_f32_e32 v98, v98
	v_exp_f32_e32 v99, v99
	v_exp_f32_e32 v100, v100
	v_exp_f32_e32 v101, v101
	v_exp_f32_e32 v102, v102
	v_exp_f32_e32 v103, v103
	v_pk_add_f32 v[104:105], v[28:29], v[12:13] neg_lo:[0,1] neg_hi:[0,1]
	v_pk_add_f32 v[106:107], v[28:29], v[14:15] neg_lo:[0,1] neg_hi:[0,1]
	v_pk_add_f32 v[108:109], v[26:27], v[10:11] op_sel:[1,0] op_sel_hi:[0,1] neg_lo:[0,1] neg_hi:[0,1]
	v_pk_add_f32 v[110:111], v[28:29], v[12:13] op_sel:[1,0] op_sel_hi:[0,1] neg_lo:[0,1] neg_hi:[0,1]
	v_pk_fma_f32 v[104:105], v[104:105], v[104:105], s[22:23] neg_lo:[1,0,0] neg_hi:[1,0,0]
	v_pk_fma_f32 v[106:107], v[106:107], v[106:107], s[28:29] neg_lo:[1,0,0] neg_hi:[1,0,0]
	v_pk_fma_f32 v[108:109], v[108:109], v[108:109], s[26:27] neg_lo:[1,0,0] neg_hi:[1,0,0]
	v_pk_fma_f32 v[110:111], v[110:111], v[110:111], s[26:27] neg_lo:[1,0,0] neg_hi:[1,0,0]
	v_exp_f32_e32 v104, v104
	v_exp_f32_e32 v105, v105
	v_exp_f32_e32 v106, v106
	v_exp_f32_e32 v107, v107
	v_exp_f32_e32 v108, v108
	v_exp_f32_e32 v109, v109
	v_exp_f32_e32 v110, v110
	v_exp_f32_e32 v111, v111
	v_pk_add_f32 v[72:73], s[30:31], v[96:97]
	v_pk_fma_f32 v[76:77], v[96:97], v[8:9], v[76:77]
	v_pk_add_f32 v[74:75], s[30:31], v[100:101]
	v_pk_add_f32 v[72:73], v[72:73], v[98:99]
	v_pk_fma_f32 v[76:77], v[98:99], v[10:11], v[76:77]
	v_pk_fma_f32 v[78:79], v[100:101], v[10:11], v[78:79]
	v_pk_add_f32 v[72:73], v[72:73], v[102:103]
	v_pk_fma_f32 v[76:77], v[102:103], v[12:13], v[76:77]
	v_pk_add_f32 v[96:97], v[26:27], v[16:17] neg_lo:[0,1] neg_hi:[0,1]
	v_pk_add_f32 v[98:99], v[24:25], v[18:19] neg_lo:[0,1] neg_hi:[0,1]
	v_pk_add_f32 v[100:101], v[26:27], v[18:19] neg_lo:[0,1] neg_hi:[0,1]
	v_pk_add_f32 v[102:103], v[28:29], v[18:19] neg_lo:[0,1] neg_hi:[0,1]
	v_pk_fma_f32 v[96:97], v[96:97], v[96:97], s[26:27] neg_lo:[1,0,0] neg_hi:[1,0,0]
	v_pk_fma_f32 v[98:99], v[98:99], v[98:99], s[26:27] neg_lo:[1,0,0] neg_hi:[1,0,0]
	v_pk_fma_f32 v[100:101], v[100:101], v[100:101], s[20:21] neg_lo:[1,0,0] neg_hi:[1,0,0]
	v_pk_fma_f32 v[102:103], v[102:103], v[102:103], s[26:27] neg_lo:[1,0,0] neg_hi:[1,0,0]
	v_exp_f32_e32 v96, v96
	v_exp_f32_e32 v97, v97
	v_exp_f32_e32 v98, v98
	v_exp_f32_e32 v99, v99
	v_exp_f32_e32 v100, v100
	v_exp_f32_e32 v101, v101
	v_exp_f32_e32 v102, v102
	v_exp_f32_e32 v103, v103
	v_pk_add_f32 v[74:75], v[74:75], v[104:105]
	v_pk_fma_f32 v[78:79], v[104:105], v[12:13], v[78:79]
	v_pk_add_f32 v[72:73], v[72:73], v[108:109] op_sel:[0,1] op_sel_hi:[1,0]
	v_pk_add_f32 v[74:75], v[74:75], v[106:107]
	v_pk_fma_f32 v[78:79], v[106:107], v[14:15], v[78:79]
	v_pk_fma_f32 v[76:77], v[108:109], v[10:11], v[76:77] op_sel:[1,1,0] op_sel_hi:[0,0,1]
	v_pk_add_f32 v[74:75], v[74:75], v[110:111] op_sel:[0,1] op_sel_hi:[1,0]
	v_pk_fma_f32 v[78:79], v[110:111], v[12:13], v[78:79] op_sel:[1,1,0] op_sel_hi:[0,0,1]
	v_pk_add_f32 v[104:105], v[26:27], v[20:21] neg_lo:[0,1] neg_hi:[0,1]
	v_pk_add_f32 v[106:107], v[28:29], v[20:21] neg_lo:[0,1] neg_hi:[0,1]
	v_pk_add_f32 v[108:109], v[30:31], v[20:21] neg_lo:[0,1] neg_hi:[0,1]
	v_pk_add_f32 v[110:111], v[28:29], v[22:23] neg_lo:[0,1] neg_hi:[0,1]
	v_pk_fma_f32 v[104:105], v[104:105], v[104:105], s[26:27] neg_lo:[1,0,0] neg_hi:[1,0,0]
	v_pk_fma_f32 v[106:107], v[106:107], v[106:107], s[20:21] neg_lo:[1,0,0] neg_hi:[1,0,0]
	v_pk_fma_f32 v[108:109], v[108:109], v[108:109], s[26:27] neg_lo:[1,0,0] neg_hi:[1,0,0]
	v_pk_fma_f32 v[110:111], v[110:111], v[110:111], s[26:27] neg_lo:[1,0,0] neg_hi:[1,0,0]
	v_exp_f32_e32 v104, v104
	v_exp_f32_e32 v105, v105
	v_exp_f32_e32 v106, v106
	v_exp_f32_e32 v107, v107
	v_exp_f32_e32 v108, v108
	v_exp_f32_e32 v109, v109
	v_exp_f32_e32 v110, v110
	v_exp_f32_e32 v111, v111
	v_pk_add_f32 v[72:73], v[72:73], v[96:97]
	v_pk_fma_f32 v[76:77], v[96:97], v[16:17], v[76:77]
	v_pk_add_f32 v[64:65], v[64:65], v[98:99]
	v_pk_fma_f32 v[68:69], v[98:99], v[24:25], v[68:69]
	v_pk_add_f32 v[72:73], v[72:73], v[100:101]
	v_pk_add_f32 v[64:65], v[64:65], v[100:101]
	v_pk_fma_f32 v[68:69], v[100:101], v[26:27], v[68:69]
	v_pk_fma_f32 v[76:77], v[100:101], v[18:19], v[76:77]
	v_pk_add_f32 v[64:65], v[64:65], v[102:103]
	v_pk_fma_f32 v[68:69], v[102:103], v[28:29], v[68:69]
	v_pk_add_f32 v[74:75], v[74:75], v[102:103]
	v_pk_fma_f32 v[78:79], v[102:103], v[18:19], v[78:79]
	v_pk_add_f32 v[96:97], v[26:27], v[18:19] op_sel:[1,0] op_sel_hi:[0,1] neg_lo:[0,1] neg_hi:[0,1]
	v_pk_add_f32 v[98:99], v[28:29], v[20:21] op_sel:[1,0] op_sel_hi:[0,1] neg_lo:[0,1] neg_hi:[0,1]
	v_pk_add_f32 v[100:101], v[26:27], v[24:25] neg_lo:[0,1] neg_hi:[0,1]
	v_pk_add_f32 v[102:103], v[28:29], v[26:27] neg_lo:[0,1] neg_hi:[0,1]
	v_pk_fma_f32 v[96:97], v[96:97], v[96:97], s[24:25] neg_lo:[1,0,0] neg_hi:[1,0,0]
	v_pk_fma_f32 v[98:99], v[98:99], v[98:99], s[24:25] neg_lo:[1,0,0] neg_hi:[1,0,0]
	v_pk_fma_f32 v[100:101], v[100:101], v[100:101], s[22:23] neg_lo:[1,0,0] neg_hi:[1,0,0]
	v_pk_fma_f32 v[102:103], v[102:103], v[102:103], s[22:23] neg_lo:[1,0,0] neg_hi:[1,0,0]
	v_exp_f32_e32 v96, v96
	v_exp_f32_e32 v97, v97
	v_exp_f32_e32 v98, v98
	v_exp_f32_e32 v99, v99
	v_exp_f32_e32 v100, v100
	v_exp_f32_e32 v101, v101
	v_exp_f32_e32 v102, v102
	v_exp_f32_e32 v103, v103
	v_pk_add_f32 v[66:67], v[66:67], v[104:105]
	v_pk_fma_f32 v[70:71], v[104:105], v[26:27], v[70:71]
	v_pk_add_f32 v[72:73], v[72:73], v[104:105]
	v_pk_fma_f32 v[76:77], v[104:105], v[20:21], v[76:77]
	v_pk_add_f32 v[66:67], v[66:67], v[106:107]
	v_pk_fma_f32 v[70:71], v[106:107], v[28:29], v[70:71]
	v_pk_add_f32 v[74:75], v[74:75], v[106:107]
	v_pk_fma_f32 v[78:79], v[106:107], v[20:21], v[78:79]
	v_pk_add_f32 v[66:67], v[66:67], v[108:109]
	v_pk_fma_f32 v[70:71], v[108:109], v[30:31], v[70:71]
	v_pk_add_f32 v[74:75], v[74:75], v[110:111]
	v_pk_fma_f32 v[78:79], v[110:111], v[22:23], v[78:79]
	v_pk_add_f32 v[104:105], v[30:31], v[28:29] neg_lo:[0,1] neg_hi:[0,1]
	v_pk_fma_f32 v[104:105], v[104:105], v[104:105], s[22:23] neg_lo:[1,0,0] neg_hi:[1,0,0]
	s_nop 0
	v_exp_f32_e32 v104, v104
	v_exp_f32_e64 v105, v105
	v_pk_add_f32 v[64:65], v[64:65], v[96:97]
	v_pk_fma_f32 v[68:69], v[96:97], v[26:27], v[68:69] op_sel:[0,1,0] op_sel_hi:[1,0,1]
	v_pk_add_f32 v[72:73], v[72:73], v[96:97] op_sel:[0,1] op_sel_hi:[1,0]
	v_pk_fma_f32 v[76:77], v[96:97], v[18:19], v[76:77] op_sel:[1,1,0] op_sel_hi:[0,0,1]
	v_pk_add_f32 v[66:67], v[66:67], v[98:99]
	v_pk_fma_f32 v[70:71], v[98:99], v[28:29], v[70:71] op_sel:[0,1,0] op_sel_hi:[1,0,1]
	v_pk_add_f32 v[74:75], v[74:75], v[98:99] op_sel:[0,1] op_sel_hi:[1,0]
	v_pk_fma_f32 v[78:79], v[98:99], v[20:21], v[78:79] op_sel:[1,1,0] op_sel_hi:[0,0,1]
	v_pk_add_f32 v[72:73], v[72:73], v[100:101]
	v_pk_fma_f32 v[76:77], v[100:101], v[24:25], v[76:77]
	v_pk_add_f32 v[74:75], v[74:75], v[102:103]
	v_pk_add_f32 v[72:73], v[72:73], v[102:103]
	v_pk_fma_f32 v[76:77], v[102:103], v[28:29], v[76:77]
	v_pk_fma_f32 v[78:79], v[102:103], v[26:27], v[78:79]
	s_nop 0
	v_sub_f32_e32 v96, v26, v9
	v_sub_f32_e32 v98, v28, v11
	v_sub_f32_e32 v100, v27, v12
	v_sub_f32_e32 v102, v29, v14
	v_sub_f32_e32 v97, v26, v17
	v_sub_f32_e32 v99, v25, v18
	v_sub_f32_e32 v101, v28, v19
	v_sub_f32_e64 v103, v27, v20
	v_fma_f32 v96, -v96, v96, s26
	v_fma_f32 v98, -v98, v98, s26
	v_fma_f32 v100, -v100, v100, s26
	v_fma_f32 v102, -v102, v102, s26
	v_fma_f32 v97, -v97, v97, s24
	v_fma_f32 v99, -v99, v99, s24
	v_fma_f32 v101, -v101, v101, s24
	v_fma_f32 v103, -v103, v103, s24
	v_exp_f32_e32 v96, v96
	v_exp_f32_e32 v98, v98
	v_exp_f32_e32 v100, v100
	v_exp_f32_e32 v102, v102
	v_exp_f32_e32 v97, v97
	v_exp_f32_e32 v99, v99
	v_exp_f32_e32 v101, v101
	v_exp_f32_e32 v103, v103
	v_pk_add_f32 v[74:75], v[74:75], v[104:105]
	v_pk_fma_f32 v[78:79], v[104:105], v[30:31], v[78:79]
	v_sub_f32_e32 v108, v30, v21
	v_sub_f32_e32 v110, v29, v22
	v_sub_f32_e32 v105, v26, v25
	v_sub_f32_e32 v104, v27, v26
	v_sub_f32_e32 v107, v28, v27
	v_sub_f32_e32 v106, v29, v28
	v_sub_f32_e64 v109, v30, v29
	v_fma_f32 v108, -v108, v108, s24
	v_fma_f32 v110, -v110, v110, s24
	v_fma_f32 v105, -v105, v105, s20
	v_fma_f32 v104, -v104, v104, s20
	v_fma_f32 v107, -v107, v107, s20
	v_fma_f32 v106, -v106, v106, s20
	v_fma_f32 v109, -v109, v109, s20
	v_exp_f32_e32 v108, v108
	v_exp_f32_e32 v110, v110
	v_exp_f32_e32 v105, v105
	v_exp_f32_e32 v104, v104
	v_exp_f32_e32 v107, v107
	v_exp_f32_e32 v106, v106
	v_exp_f32_e32 v109, v109
	v_add_f32_e32 v72, v72, v96
	v_fmac_f32_e32 v76, v96, v9
	v_add_f32_e32 v74, v74, v98
	v_fmac_f32_e32 v78, v98, v11
	v_add_f32_e32 v73, v73, v100
	v_fmac_f32_e32 v77, v100, v12
	v_add_f32_e32 v75, v75, v102
	v_fmac_f32_e32 v79, v102, v14
	v_add_f32_e32 v72, v72, v97
	v_fmac_f32_e32 v76, v97, v17
	v_add_f32_e32 v64, v64, v99
	v_fmac_f32_e32 v68, v99, v25
	v_add_f32_e32 v65, v65, v101
	v_fmac_f32_e32 v69, v101, v28
	v_add_f32_e32 v74, v74, v101
	v_fmac_f32_e32 v78, v101, v19
	v_add_f32_e32 v66, v66, v103
	v_fmac_f32_e32 v70, v103, v27
	v_add_f32_e32 v73, v73, v103
	v_fmac_f32_e32 v77, v103, v20
	v_add_f32_e32 v67, v67, v108
	v_fmac_f32_e32 v71, v108, v30
	v_add_f32_e32 v75, v75, v110
	v_fmac_f32_e32 v79, v110, v22
	v_add_f32_e32 v72, v72, v105
	v_fmac_f32_e32 v76, v105, v25
	v_add_f32_e32 v73, v73, v107
	v_fmac_f32_e32 v77, v107, v28
	v_add_f32_e32 v74, v74, v107
	v_fmac_f32_e32 v78, v107, v27
	v_add_f32_e32 v75, v75, v109
	v_fmac_f32_e64 v79, v109, v30
	v_pk_add_f32 v[72:73], v[72:73], v[104:105] op_sel_hi:[1,0]
	v_pk_fma_f32 v[76:77], v[104:105], v[26:27], v[76:77] op_sel:[0,1,0] op_sel_hi:[0,0,1]
	v_pk_add_f32 v[74:75], v[74:75], v[106:107] op_sel_hi:[1,0]
	v_pk_fma_f32 v[78:79], v[106:107], v[28:29], v[78:79] op_sel:[0,1,0] op_sel_hi:[0,0,1]
	s_waitcnt vmcnt(9)
	s_nop 0
	v_mov_b32_dpp v32, v36 row_shr:1 row_mask:0xf bank_mask:0xf
	v_mov_b32_dpp v33, v37 row_shr:1 row_mask:0xf bank_mask:0xf
	v_mov_b32_dpp v38, v34 row_shl:1 row_mask:0xf bank_mask:0xf
	v_mov_b32_dpp v39, v35 row_shl:1 row_mask:0xf bank_mask:0xf
	v_pk_mul_f32 v[34:35], v[34:35], s[32:33]
	v_pk_mul_f32 v[36:37], v[36:37], s[32:33]
	v_cndmask_b32_e64 v33, v33, v32, vcc
	v_cndmask_b32_e64 v38, v38, v39, s[16:17]
	v_pk_mul_f32 v[84:85], v[34:35], s[30:31]
	v_pk_mul_f32 v[86:87], v[36:37], s[30:31]
	v_pk_mul_f32 v[32:33], v[32:33], s[32:33]
	v_pk_mul_f32 v[38:39], v[38:39], s[32:33]
	s_setprio 2
	s_nop 0
	v_pk_add_f32 v[96:97], v[34:35], v[16:17] neg_lo:[0,1] neg_hi:[0,1]
	v_pk_add_f32 v[98:99], v[32:33], v[18:19] neg_lo:[0,1] neg_hi:[0,1]
	v_pk_add_f32 v[100:101], v[34:35], v[18:19] neg_lo:[0,1] neg_hi:[0,1]
	v_pk_add_f32 v[102:103], v[36:37], v[18:19] neg_lo:[0,1] neg_hi:[0,1]
	v_pk_fma_f32 v[96:97], v[96:97], v[96:97], s[28:29] neg_lo:[1,0,0] neg_hi:[1,0,0]
	v_pk_fma_f32 v[98:99], v[98:99], v[98:99], s[28:29] neg_lo:[1,0,0] neg_hi:[1,0,0]
	v_pk_fma_f32 v[100:101], v[100:101], v[100:101], s[22:23] neg_lo:[1,0,0] neg_hi:[1,0,0]
	v_pk_fma_f32 v[102:103], v[102:103], v[102:103], s[28:29] neg_lo:[1,0,0] neg_hi:[1,0,0]
	v_exp_f32_e32 v96, v96
	v_exp_f32_e32 v97, v97
	v_exp_f32_e32 v98, v98
	v_exp_f32_e32 v99, v99
	v_exp_f32_e32 v100, v100
	v_exp_f32_e32 v101, v101
	v_exp_f32_e32 v102, v102
	v_exp_f32_e32 v103, v103
	v_pk_add_f32 v[104:105], v[34:35], v[20:21] neg_lo:[0,1] neg_hi:[0,1]
	v_pk_add_f32 v[106:107], v[36:37], v[20:21] neg_lo:[0,1] neg_hi:[0,1]
	v_pk_add_f32 v[108:109], v[38:39], v[20:21] neg_lo:[0,1] neg_hi:[0,1]
	v_pk_add_f32 v[110:111], v[36:37], v[22:23] neg_lo:[0,1] neg_hi:[0,1]
	v_pk_fma_f32 v[104:105], v[104:105], v[104:105], s[28:29] neg_lo:[1,0,0] neg_hi:[1,0,0]
	v_pk_fma_f32 v[106:107], v[106:107], v[106:107], s[22:23] neg_lo:[1,0,0] neg_hi:[1,0,0]
	v_pk_fma_f32 v[108:109], v[108:109], v[108:109], s[28:29] neg_lo:[1,0,0] neg_hi:[1,0,0]
	v_pk_fma_f32 v[110:111], v[110:111], v[110:111], s[28:29] neg_lo:[1,0,0] neg_hi:[1,0,0]
	v_exp_f32_e32 v104, v104
	v_exp_f32_e32 v105, v105
	v_exp_f32_e32 v106, v106
	v_exp_f32_e32 v107, v107
	v_exp_f32_e32 v108, v108
	v_exp_f32_e32 v109, v109
	v_exp_f32_e32 v110, v110
	v_exp_f32_e32 v111, v111
	v_pk_add_f32 v[80:81], s[30:31], v[96:97]
	v_pk_fma_f32 v[84:85], v[96:97], v[16:17], v[84:85]
	v_pk_add_f32 v[64:65], v[64:65], v[98:99]
	v_pk_fma_f32 v[68:69], v[98:99], v[32:33], v[68:69]
	v_pk_add_f32 v[80:81], v[80:81], v[100:101]
	v_pk_add_f32 v[64:65], v[64:65], v[100:101]
	v_pk_fma_f32 v[68:69], v[100:101], v[34:35], v[68:69]
	v_pk_fma_f32 v[84:85], v[100:101], v[18:19], v[84:85]
	v_pk_add_f32 v[64:65], v[64:65], v[102:103]
	v_pk_fma_f32 v[68:69], v[102:103], v[36:37], v[68:69]
	v_pk_add_f32 v[82:83], s[30:31], v[102:103]
	v_pk_fma_f32 v[86:87], v[102:103], v[18:19], v[86:87]
	v_pk_add_f32 v[96:97], v[34:35], v[18:19] op_sel:[1,0] op_sel_hi:[0,1] neg_lo:[0,1] neg_hi:[0,1]
	v_pk_add_f32 v[98:99], v[36:37], v[20:21] op_sel:[1,0] op_sel_hi:[0,1] neg_lo:[0,1] neg_hi:[0,1]
	v_pk_add_f32 v[100:101], v[34:35], v[24:25] neg_lo:[0,1] neg_hi:[0,1]
	v_pk_add_f32 v[102:103], v[32:33], v[26:27] neg_lo:[0,1] neg_hi:[0,1]
	v_pk_fma_f32 v[96:97], v[96:97], v[96:97], s[26:27] neg_lo:[1,0,0] neg_hi:[1,0,0]
	v_pk_fma_f32 v[98:99], v[98:99], v[98:99], s[26:27] neg_lo:[1,0,0] neg_hi:[1,0,0]
	v_pk_fma_f32 v[100:101], v[100:101], v[100:101], s[26:27] neg_lo:[1,0,0] neg_hi:[1,0,0]
	v_pk_fma_f32 v[102:103], v[102:103], v[102:103], s[26:27] neg_lo:[1,0,0] neg_hi:[1,0,0]
	v_exp_f32_e32 v96, v96
	v_exp_f32_e32 v97, v97
	v_exp_f32_e32 v98, v98
	v_exp_f32_e32 v99, v99
	v_exp_f32_e32 v100, v100
	v_exp_f32_e32 v101, v101
	v_exp_f32_e32 v102, v102
	v_exp_f32_e32 v103, v103
	v_pk_add_f32 v[66:67], v[66:67], v[104:105]
	v_pk_fma_f32 v[70:71], v[104:105], v[34:35], v[70:71]
	v_pk_add_f32 v[80:81], v[80:81], v[104:105]
	v_pk_fma_f32 v[84:85], v[104:105], v[20:21], v[84:85]
	v_pk_add_f32 v[66:67], v[66:67], v[106:107]
	v_pk_fma_f32 v[70:71], v[106:107], v[36:37], v[70:71]
	v_pk_add_f32 v[82:83], v[82:83], v[106:107]
	v_pk_fma_f32 v[86:87], v[106:107], v[20:21], v[86:87]
	v_pk_add_f32 v[66:67], v[66:67], v[108:109]
	v_pk_fma_f32 v[70:71], v[108:109], v[38:39], v[70:71]
	v_pk_add_f32 v[82:83], v[82:83], v[110:111]
	v_pk_fma_f32 v[86:87], v[110:111], v[22:23], v[86:87]
	v_pk_add_f32 v[104:105], v[34:35], v[26:27] neg_lo:[0,1] neg_hi:[0,1]
	v_pk_add_f32 v[106:107], v[36:37], v[26:27] neg_lo:[0,1] neg_hi:[0,1]
	v_pk_add_f32 v[108:109], v[34:35], v[28:29] neg_lo:[0,1] neg_hi:[0,1]
	v_pk_add_f32 v[110:111], v[36:37], v[28:29] neg_lo:[0,1] neg_hi:[0,1]
	v_pk_fma_f32 v[104:105], v[104:105], v[104:105], s[20:21] neg_lo:[1,0,0] neg_hi:[1,0,0]
	v_pk_fma_f32 v[106:107], v[106:107], v[106:107], s[26:27] neg_lo:[1,0,0] neg_hi:[1,0,0]
	v_pk_fma_f32 v[108:109], v[108:109], v[108:109], s[26:27] neg_lo:[1,0,0] neg_hi:[1,0,0]
	v_pk_fma_f32 v[110:111], v[110:111], v[110:111], s[20:21] neg_lo:[1,0,0] neg_hi:[1,0,0]
	v_exp_f32_e32 v104, v104
	v_exp_f32_e32 v105, v105
	v_exp_f32_e32 v106, v106
	v_exp_f32_e32 v107, v107
	v_exp_f32_e32 v108, v108
	v_exp_f32_e32 v109, v109
	v_exp_f32_e32 v110, v110
	v_exp_f32_e32 v111, v111
	v_pk_add_f32 v[64:65], v[64:65], v[96:97]
	v_pk_fma_f32 v[68:69], v[96:97], v[34:35], v[68:69] op_sel:[0,1,0] op_sel_hi:[1,0,1]
	v_pk_add_f32 v[80:81], v[80:81], v[96:97] op_sel:[0,1] op_sel_hi:[1,0]
	v_pk_fma_f32 v[84:85], v[96:97], v[18:19], v[84:85] op_sel:[1,1,0] op_sel_hi:[0,0,1]
	v_pk_add_f32 v[66:67], v[66:67], v[98:99]
	v_pk_fma_f32 v[70:71], v[98:99], v[36:37], v[70:71] op_sel:[0,1,0] op_sel_hi:[1,0,1]
	v_pk_add_f32 v[82:83], v[82:83], v[98:99] op_sel:[0,1] op_sel_hi:[1,0]
	v_pk_fma_f32 v[86:87], v[98:99], v[20:21], v[86:87] op_sel:[1,1,0] op_sel_hi:[0,0,1]
	v_pk_add_f32 v[80:81], v[80:81], v[100:101]
	v_pk_fma_f32 v[84:85], v[100:101], v[24:25], v[84:85]
	v_pk_add_f32 v[72:73], v[72:73], v[102:103]
	v_pk_fma_f32 v[76:77], v[102:103], v[32:33], v[76:77]
	v_pk_add_f32 v[96:97], v[38:39], v[28:29] neg_lo:[0,1] neg_hi:[0,1]
	v_pk_add_f32 v[98:99], v[36:37], v[30:31] neg_lo:[0,1] neg_hi:[0,1]
	v_pk_add_f32 v[100:101], v[34:35], v[26:27] op_sel:[1,0] op_sel_hi:[0,1] neg_lo:[0,1] neg_hi:[0,1]
	v_pk_add_f32 v[102:103], v[36:37], v[28:29] op_sel:[1,0] op_sel_hi:[0,1] neg_lo:[0,1] neg_hi:[0,1]
	v_pk_fma_f32 v[96:97], v[96:97], v[96:97], s[26:27] neg_lo:[1,0,0] neg_hi:[1,0,0]
	v_pk_fma_f32 v[98:99], v[98:99], v[98:99], s[26:27] neg_lo:[1,0,0] neg_hi:[1,0,0]
	v_pk_fma_f32 v[100:101], v[100:101], v[100:101], s[24:25] neg_lo:[1,0,0] neg_hi:[1,0,0]
	v_pk_fma_f32 v[102:103], v[102:103], v[102:103], s[24:25] neg_lo:[1,0,0] neg_hi:[1,0,0]
	v_exp_f32_e32 v96, v96
	v_exp_f32_e32 v97, v97
	v_exp_f32_e32 v98, v98
	v_exp_f32_e32 v99, v99
	v_exp_f32_e32 v100, v100
	v_exp_f32_e32 v101, v101
	v_exp_f32_e32 v102, v102
	v_exp_f32_e32 v103, v103
	v_pk_add_f32 v[72:73], v[72:73], v[104:105]
	v_pk_fma_f32 v[76:77], v[104:105], v[34:35], v[76:77]
	v_pk_add_f32 v[80:81], v[80:81], v[104:105]
	v_pk_fma_f32 v[84:85], v[104:105], v[26:27], v[84:85]
	v_pk_add_f32 v[72:73], v[72:73], v[106:107]
	v_pk_fma_f32 v[76:77], v[106:107], v[36:37], v[76:77]
	v_pk_add_f32 v[82:83], v[82:83], v[106:107]
	v_pk_fma_f32 v[86:87], v[106:107], v[26:27], v[86:87]
	v_pk_add_f32 v[74:75], v[74:75], v[108:109]
	v_pk_fma_f32 v[78:79], v[108:109], v[34:35], v[78:79]
	v_pk_add_f32 v[80:81], v[80:81], v[108:109]
	v_pk_fma_f32 v[84:85], v[108:109], v[28:29], v[84:85]
	v_pk_add_f32 v[74:75], v[74:75], v[110:111]
	v_pk_fma_f32 v[78:79], v[110:111], v[36:37], v[78:79]
	v_pk_add_f32 v[82:83], v[82:83], v[110:111]
	v_pk_fma_f32 v[86:87], v[110:111], v[28:29], v[86:87]
	v_pk_add_f32 v[104:105], v[34:35], v[32:33] neg_lo:[0,1] neg_hi:[0,1]
	v_pk_add_f32 v[106:107], v[36:37], v[34:35] neg_lo:[0,1] neg_hi:[0,1]
	v_pk_add_f32 v[108:109], v[38:39], v[36:37] neg_lo:[0,1] neg_hi:[0,1]
	v_pk_fma_f32 v[104:105], v[104:105], v[104:105], s[22:23] neg_lo:[1,0,0] neg_hi:[1,0,0]
	v_pk_fma_f32 v[106:107], v[106:107], v[106:107], s[22:23] neg_lo:[1,0,0] neg_hi:[1,0,0]
	v_pk_fma_f32 v[108:109], v[108:109], v[108:109], s[22:23] neg_lo:[1,0,0] neg_hi:[1,0,0]
	v_exp_f32_e32 v104, v104
	v_exp_f32_e32 v105, v105
	v_exp_f32_e32 v106, v106
	v_exp_f32_e32 v107, v107
	v_exp_f32_e32 v108, v108
	v_exp_f32_e32 v109, v109
	v_pk_add_f32 v[74:75], v[74:75], v[96:97]
	v_pk_fma_f32 v[78:79], v[96:97], v[38:39], v[78:79]
	v_pk_add_f32 v[82:83], v[82:83], v[98:99]
	v_pk_fma_f32 v[86:87], v[98:99], v[30:31], v[86:87]
	v_pk_add_f32 v[72:73], v[72:73], v[100:101]
	v_pk_fma_f32 v[76:77], v[100:101], v[34:35], v[76:77] op_sel:[0,1,0] op_sel_hi:[1,0,1]
	v_pk_add_f32 v[80:81], v[80:81], v[100:101] op_sel:[0,1] op_sel_hi:[1,0]
	v_pk_fma_f32 v[84:85], v[100:101], v[26:27], v[84:85] op_sel:[1,1,0] op_sel_hi:[0,0,1]
	v_pk_add_f32 v[74:75], v[74:75], v[102:103]
	v_pk_fma_f32 v[78:79], v[102:103], v[36:37], v[78:79] op_sel:[0,1,0] op_sel_hi:[1,0,1]
	v_pk_add_f32 v[82:83], v[82:83], v[102:103] op_sel:[0,1] op_sel_hi:[1,0]
	v_pk_fma_f32 v[86:87], v[102:103], v[28:29], v[86:87] op_sel:[1,1,0] op_sel_hi:[0,0,1]
	v_sub_f32_e32 v96, v34, v17
	v_sub_f32_e32 v98, v33, v18
	v_sub_f32_e32 v100, v36, v19
	v_sub_f32_e32 v102, v35, v20
	v_sub_f32_e32 v97, v38, v21
	v_sub_f32_e32 v99, v37, v22
	v_sub_f32_e32 v101, v34, v25
	v_sub_f32_e32 v103, v33, v26
	v_fma_f32 v96, -v96, v96, s26
	v_fma_f32 v98, -v98, v98, s26
	v_fma_f32 v100, -v100, v100, s26
	v_fma_f32 v102, -v102, v102, s26
	v_fma_f32 v97, -v97, v97, s26
	v_fma_f32 v99, -v99, v99, s26
	v_fma_f32 v101, -v101, v101, s24
	v_fma_f32 v103, -v103, v103, s24
	v_exp_f32_e32 v96, v96
	v_exp_f32_e32 v98, v98
	v_exp_f32_e32 v100, v100
	v_exp_f32_e32 v102, v102
	v_exp_f32_e32 v97, v97
	v_exp_f32_e32 v99, v99
	v_exp_f32_e32 v101, v101
	v_exp_f32_e32 v103, v103
	v_pk_add_f32 v[80:81], v[80:81], v[104:105]
	v_pk_fma_f32 v[84:85], v[104:105], v[32:33], v[84:85]
	v_pk_add_f32 v[82:83], v[82:83], v[106:107]
	v_pk_add_f32 v[80:81], v[80:81], v[106:107]
	v_pk_fma_f32 v[84:85], v[106:107], v[36:37], v[84:85]
	v_pk_fma_f32 v[86:87], v[106:107], v[34:35], v[86:87]
	v_pk_add_f32 v[82:83], v[82:83], v[108:109]
	v_pk_fma_f32 v[86:87], v[108:109], v[38:39], v[86:87]
	v_sub_f32_e32 v108, v36, v27
	v_sub_f32_e32 v110, v35, v28
	v_sub_f32_e32 v105, v38, v29
	v_sub_f32_e32 v107, v37, v30
	v_sub_f32_e32 v109, v34, v33
	v_sub_f32_e32 v104, v35, v34
	v_sub_f32_e32 v111, v36, v35
	v_sub_f32_e32 v106, v37, v36
	v_fma_f32 v108, -v108, v108, s24
	v_fma_f32 v110, -v110, v110, s24
	v_fma_f32 v105, -v105, v105, s24
	v_fma_f32 v107, -v107, v107, s24
	v_fma_f32 v109, -v109, v109, s20
	v_fma_f32 v104, -v104, v104, s20
	v_fma_f32 v111, -v111, v111, s20
	v_fma_f32 v106, -v106, v106, s20
	v_exp_f32_e32 v108, v108
	v_exp_f32_e32 v110, v110
	v_exp_f32_e32 v105, v105
	v_exp_f32_e32 v107, v107
	v_exp_f32_e32 v109, v109
	v_exp_f32_e32 v104, v104
	v_exp_f32_e32 v111, v111
	v_exp_f32_e32 v106, v106
	v_add_f32_e32 v80, v80, v96
	v_fmac_f32_e32 v84, v96, v17
	v_add_f32_e32 v64, v64, v98
	v_fmac_f32_e32 v68, v98, v33
	v_add_f32_e32 v65, v65, v100
	v_fmac_f32_e32 v69, v100, v36
	v_add_f32_e32 v82, v82, v100
	v_fmac_f32_e32 v86, v100, v19
	v_add_f32_e32 v66, v66, v102
	v_fmac_f32_e32 v70, v102, v35
	v_add_f32_e32 v81, v81, v102
	v_fmac_f32_e32 v85, v102, v20
	v_add_f32_e32 v67, v67, v97
	v_fmac_f32_e32 v71, v97, v38
	v_add_f32_e32 v83, v83, v99
	v_fmac_f32_e32 v87, v99, v22
	v_add_f32_e32 v80, v80, v101
	v_fmac_f32_e32 v84, v101, v25
	v_add_f32_e32 v72, v72, v103
	v_fmac_f32_e32 v76, v103, v33
	v_sub_f32_e64 v96, v38, v37
	v_fma_f32 v96, -v96, v96, s20
	s_nop 0
	v_exp_f32_e32 v96, v96
	v_add_f32_e32 v73, v73, v108
	v_fmac_f32_e32 v77, v108, v36
	v_add_f32_e32 v82, v82, v108
	v_fmac_f32_e32 v86, v108, v27
	v_add_f32_e32 v74, v74, v110
	v_fmac_f32_e32 v78, v110, v35
	v_add_f32_e32 v81, v81, v110
	v_fmac_f32_e32 v85, v110, v28
	v_add_f32_e32 v75, v75, v105
	v_fmac_f32_e32 v79, v105, v38
	v_add_f32_e32 v83, v83, v107
	v_fmac_f32_e32 v87, v107, v30
	v_add_f32_e32 v80, v80, v109
	v_fmac_f32_e32 v84, v109, v33
	v_add_f32_e32 v81, v81, v111
	v_fmac_f32_e32 v85, v111, v36
	v_add_f32_e32 v82, v82, v111
	v_fmac_f32_e32 v86, v111, v35
	v_pk_add_f32 v[80:81], v[80:81], v[104:105] op_sel_hi:[1,0]
	v_pk_fma_f32 v[84:85], v[104:105], v[34:35], v[84:85] op_sel:[0,1,0] op_sel_hi:[0,0,1]
	v_pk_add_f32 v[82:83], v[82:83], v[106:107] op_sel_hi:[1,0]
	v_pk_fma_f32 v[86:87], v[106:107], v[36:37], v[86:87] op_sel:[0,1,0] op_sel_hi:[0,0,1]
	s_nop 0
	v_add_f32_e32 v83, v83, v96
	v_fmac_f32_e32 v87, v96, v38
	v_rcp_f32_e32 v96, v64
	v_rcp_f32_e32 v97, v65
	v_rcp_f32_e32 v98, v66
	v_rcp_f32_e64 v99, v67
	v_pk_mul_f32 v[68:69], v[68:69], s[34:35]
	v_pk_mul_f32 v[70:71], v[70:71], s[34:35]
	v_pk_mul_f32 v[68:69], v[68:69], v[96:97]
	v_pk_mul_f32 v[70:71], v[70:71], v[98:99]
	buffer_store_dwordx4 v[68:71], v114, s[12:15], 0 offen sc1
	s_waitcnt vmcnt(7)
	s_nop 0
	v_mov_b32_dpp v40, v44 row_shr:1 row_mask:0xf bank_mask:0xf
	v_mov_b32_dpp v41, v45 row_shr:1 row_mask:0xf bank_mask:0xf
	v_mov_b32_dpp v46, v42 row_shl:1 row_mask:0xf bank_mask:0xf
	v_mov_b32_dpp v47, v43 row_shl:1 row_mask:0xf bank_mask:0xf
	v_pk_mul_f32 v[42:43], v[42:43], s[32:33]
	v_pk_mul_f32 v[44:45], v[44:45], s[32:33]
	v_cndmask_b32_e64 v41, v41, v40, vcc
	v_cndmask_b32_e64 v46, v46, v47, s[16:17]
	v_pk_mul_f32 v[92:93], v[42:43], s[30:31]
	v_pk_mul_f32 v[94:95], v[44:45], s[30:31]
	v_pk_mul_f32 v[40:41], v[40:41], s[32:33]
	v_pk_mul_f32 v[46:47], v[46:47], s[32:33]
	s_setprio 1
	s_nop 0
	v_pk_add_f32 v[96:97], v[42:43], v[24:25] neg_lo:[0,1] neg_hi:[0,1]
	v_pk_add_f32 v[98:99], v[40:41], v[26:27] neg_lo:[0,1] neg_hi:[0,1]
	v_pk_add_f32 v[100:101], v[42:43], v[26:27] neg_lo:[0,1] neg_hi:[0,1]
	v_pk_add_f32 v[102:103], v[44:45], v[26:27] neg_lo:[0,1] neg_hi:[0,1]
	v_pk_fma_f32 v[96:97], v[96:97], v[96:97], s[28:29] neg_lo:[1,0,0] neg_hi:[1,0,0]
	v_pk_fma_f32 v[98:99], v[98:99], v[98:99], s[28:29] neg_lo:[1,0,0] neg_hi:[1,0,0]
	v_pk_fma_f32 v[100:101], v[100:101], v[100:101], s[22:23] neg_lo:[1,0,0] neg_hi:[1,0,0]
	v_pk_fma_f32 v[102:103], v[102:103], v[102:103], s[28:29] neg_lo:[1,0,0] neg_hi:[1,0,0]
	v_exp_f32_e32 v96, v96
	v_exp_f32_e32 v97, v97
	v_exp_f32_e32 v98, v98
	v_exp_f32_e32 v99, v99
	v_exp_f32_e32 v100, v100
	v_exp_f32_e32 v101, v101
	v_exp_f32_e32 v102, v102
	v_exp_f32_e32 v103, v103
	v_pk_add_f32 v[104:105], v[42:43], v[28:29] neg_lo:[0,1] neg_hi:[0,1]
	v_pk_add_f32 v[106:107], v[44:45], v[28:29] neg_lo:[0,1] neg_hi:[0,1]
	v_pk_add_f32 v[108:109], v[46:47], v[28:29] neg_lo:[0,1] neg_hi:[0,1]
	v_pk_add_f32 v[110:111], v[44:45], v[30:31] neg_lo:[0,1] neg_hi:[0,1]
	v_pk_fma_f32 v[104:105], v[104:105], v[104:105], s[28:29] neg_lo:[1,0,0] neg_hi:[1,0,0]
	v_pk_fma_f32 v[106:107], v[106:107], v[106:107], s[22:23] neg_lo:[1,0,0] neg_hi:[1,0,0]
	v_pk_fma_f32 v[108:109], v[108:109], v[108:109], s[28:29] neg_lo:[1,0,0] neg_hi:[1,0,0]
	v_pk_fma_f32 v[110:111], v[110:111], v[110:111], s[28:29] neg_lo:[1,0,0] neg_hi:[1,0,0]
	v_exp_f32_e32 v104, v104
	v_exp_f32_e32 v105, v105
	v_exp_f32_e32 v106, v106
	v_exp_f32_e32 v107, v107
	v_exp_f32_e32 v108, v108
	v_exp_f32_e32 v109, v109
	v_exp_f32_e32 v110, v110
	v_exp_f32_e32 v111, v111
	v_pk_add_f32 v[88:89], s[30:31], v[96:97]
	v_pk_fma_f32 v[92:93], v[96:97], v[24:25], v[92:93]
	v_pk_add_f32 v[72:73], v[72:73], v[98:99]
	v_pk_fma_f32 v[76:77], v[98:99], v[40:41], v[76:77]
	v_pk_add_f32 v[88:89], v[88:89], v[100:101]
	v_pk_add_f32 v[72:73], v[72:73], v[100:101]
	v_pk_fma_f32 v[76:77], v[100:101], v[42:43], v[76:77]
	v_pk_fma_f32 v[92:93], v[100:101], v[26:27], v[92:93]
	v_pk_add_f32 v[72:73], v[72:73], v[102:103]
	v_pk_fma_f32 v[76:77], v[102:103], v[44:45], v[76:77]
	v_pk_add_f32 v[90:91], s[30:31], v[102:103]
	v_pk_fma_f32 v[94:95], v[102:103], v[26:27], v[94:95]
	v_pk_add_f32 v[96:97], v[42:43], v[26:27] op_sel:[1,0] op_sel_hi:[0,1] neg_lo:[0,1] neg_hi:[0,1]
	v_pk_add_f32 v[98:99], v[44:45], v[28:29] op_sel:[1,0] op_sel_hi:[0,1] neg_lo:[0,1] neg_hi:[0,1]
	v_pk_add_f32 v[100:101], v[42:43], v[32:33] neg_lo:[0,1] neg_hi:[0,1]
	v_pk_add_f32 v[102:103], v[40:41], v[34:35] neg_lo:[0,1] neg_hi:[0,1]
	v_pk_fma_f32 v[96:97], v[96:97], v[96:97], s[26:27] neg_lo:[1,0,0] neg_hi:[1,0,0]
	v_pk_fma_f32 v[98:99], v[98:99], v[98:99], s[26:27] neg_lo:[1,0,0] neg_hi:[1,0,0]
	v_pk_fma_f32 v[100:101], v[100:101], v[100:101], s[26:27] neg_lo:[1,0,0] neg_hi:[1,0,0]
	v_pk_fma_f32 v[102:103], v[102:103], v[102:103], s[26:27] neg_lo:[1,0,0] neg_hi:[1,0,0]
	v_exp_f32_e32 v96, v96
	v_exp_f32_e32 v97, v97
	v_exp_f32_e32 v98, v98
	v_exp_f32_e32 v99, v99
	v_exp_f32_e32 v100, v100
	v_exp_f32_e32 v101, v101
	v_exp_f32_e32 v102, v102
	v_exp_f32_e32 v103, v103
	v_pk_add_f32 v[74:75], v[74:75], v[104:105]
	v_pk_fma_f32 v[78:79], v[104:105], v[42:43], v[78:79]
	v_pk_add_f32 v[88:89], v[88:89], v[104:105]
	v_pk_fma_f32 v[92:93], v[104:105], v[28:29], v[92:93]
	v_pk_add_f32 v[74:75], v[74:75], v[106:107]
	v_pk_fma_f32 v[78:79], v[106:107], v[44:45], v[78:79]
	v_pk_add_f32 v[90:91], v[90:91], v[106:107]
	v_pk_fma_f32 v[94:95], v[106:107], v[28:29], v[94:95]
	v_pk_add_f32 v[74:75], v[74:75], v[108:109]
	v_pk_fma_f32 v[78:79], v[108:109], v[46:47], v[78:79]
	v_pk_add_f32 v[90:91], v[90:91], v[110:111]
	v_pk_fma_f32 v[94:95], v[110:111], v[30:31], v[94:95]
	v_pk_add_f32 v[104:105], v[42:43], v[34:35] neg_lo:[0,1] neg_hi:[0,1]
	v_pk_add_f32 v[106:107], v[44:45], v[34:35] neg_lo:[0,1] neg_hi:[0,1]
	v_pk_add_f32 v[108:109], v[42:43], v[36:37] neg_lo:[0,1] neg_hi:[0,1]
	v_pk_add_f32 v[110:111], v[44:45], v[36:37] neg_lo:[0,1] neg_hi:[0,1]
	v_pk_fma_f32 v[104:105], v[104:105], v[104:105], s[20:21] neg_lo:[1,0,0] neg_hi:[1,0,0]
	v_pk_fma_f32 v[106:107], v[106:107], v[106:107], s[26:27] neg_lo:[1,0,0] neg_hi:[1,0,0]
	v_pk_fma_f32 v[108:109], v[108:109], v[108:109], s[26:27] neg_lo:[1,0,0] neg_hi:[1,0,0]
	v_pk_fma_f32 v[110:111], v[110:111], v[110:111], s[20:21] neg_lo:[1,0,0] neg_hi:[1,0,0]
	v_exp_f32_e32 v104, v104
	v_exp_f32_e32 v105, v105
	v_exp_f32_e32 v106, v106
	v_exp_f32_e32 v107, v107
	v_exp_f32_e32 v108, v108
	v_exp_f32_e32 v109, v109
	v_exp_f32_e32 v110, v110
	v_exp_f32_e32 v111, v111
	v_pk_add_f32 v[72:73], v[72:73], v[96:97]
	v_pk_fma_f32 v[76:77], v[96:97], v[42:43], v[76:77] op_sel:[0,1,0] op_sel_hi:[1,0,1]
	v_pk_add_f32 v[88:89], v[88:89], v[96:97] op_sel:[0,1] op_sel_hi:[1,0]
	v_pk_fma_f32 v[92:93], v[96:97], v[26:27], v[92:93] op_sel:[1,1,0] op_sel_hi:[0,0,1]
	v_pk_add_f32 v[74:75], v[74:75], v[98:99]
	v_pk_fma_f32 v[78:79], v[98:99], v[44:45], v[78:79] op_sel:[0,1,0] op_sel_hi:[1,0,1]
	v_pk_add_f32 v[90:91], v[90:91], v[98:99] op_sel:[0,1] op_sel_hi:[1,0]
	v_pk_fma_f32 v[94:95], v[98:99], v[28:29], v[94:95] op_sel:[1,1,0] op_sel_hi:[0,0,1]
	v_pk_add_f32 v[88:89], v[88:89], v[100:101]
	v_pk_fma_f32 v[92:93], v[100:101], v[32:33], v[92:93]
	v_pk_add_f32 v[80:81], v[80:81], v[102:103]
	v_pk_fma_f32 v[84:85], v[102:103], v[40:41], v[84:85]
	v_pk_add_f32 v[96:97], v[46:47], v[36:37] neg_lo:[0,1] neg_hi:[0,1]
	v_pk_add_f32 v[98:99], v[44:45], v[38:39] neg_lo:[0,1] neg_hi:[0,1]
	v_pk_add_f32 v[100:101], v[42:43], v[34:35] op_sel:[1,0] op_sel_hi:[0,1] neg_lo:[0,1] neg_hi:[0,1]
	v_pk_add_f32 v[102:103], v[44:45], v[36:37] op_sel:[1,0] op_sel_hi:[0,1] neg_lo:[0,1] neg_hi:[0,1]
	v_pk_fma_f32 v[96:97], v[96:97], v[96:97], s[26:27] neg_lo:[1,0,0] neg_hi:[1,0,0]
	v_pk_fma_f32 v[98:99], v[98:99], v[98:99], s[26:27] neg_lo:[1,0,0] neg_hi:[1,0,0]
	v_pk_fma_f32 v[100:101], v[100:101], v[100:101], s[24:25] neg_lo:[1,0,0] neg_hi:[1,0,0]
	v_pk_fma_f32 v[102:103], v[102:103], v[102:103], s[24:25] neg_lo:[1,0,0] neg_hi:[1,0,0]
	v_exp_f32_e32 v96, v96
	v_exp_f32_e32 v97, v97
	v_exp_f32_e32 v98, v98
	v_exp_f32_e32 v99, v99
	v_exp_f32_e32 v100, v100
	v_exp_f32_e32 v101, v101
	v_exp_f32_e32 v102, v102
	v_exp_f32_e32 v103, v103
	v_pk_add_f32 v[80:81], v[80:81], v[104:105]
	v_pk_fma_f32 v[84:85], v[104:105], v[42:43], v[84:85]
	v_pk_add_f32 v[88:89], v[88:89], v[104:105]
	v_pk_fma_f32 v[92:93], v[104:105], v[34:35], v[92:93]
	v_pk_add_f32 v[80:81], v[80:81], v[106:107]
	v_pk_fma_f32 v[84:85], v[106:107], v[44:45], v[84:85]
	v_pk_add_f32 v[90:91], v[90:91], v[106:107]
	v_pk_fma_f32 v[94:95], v[106:107], v[34:35], v[94:95]
	v_pk_add_f32 v[82:83], v[82:83], v[108:109]
	v_pk_fma_f32 v[86:87], v[108:109], v[42:43], v[86:87]
	v_pk_add_f32 v[88:89], v[88:89], v[108:109]
	v_pk_fma_f32 v[92:93], v[108:109], v[36:37], v[92:93]
	v_pk_add_f32 v[82:83], v[82:83], v[110:111]
	v_pk_fma_f32 v[86:87], v[110:111], v[44:45], v[86:87]
	v_pk_add_f32 v[90:91], v[90:91], v[110:111]
	v_pk_fma_f32 v[94:95], v[110:111], v[36:37], v[94:95]
	v_pk_add_f32 v[104:105], v[42:43], v[40:41] neg_lo:[0,1] neg_hi:[0,1]
	v_pk_add_f32 v[106:107], v[44:45], v[42:43] neg_lo:[0,1] neg_hi:[0,1]
	v_pk_add_f32 v[108:109], v[46:47], v[44:45] neg_lo:[0,1] neg_hi:[0,1]
	v_pk_fma_f32 v[104:105], v[104:105], v[104:105], s[22:23] neg_lo:[1,0,0] neg_hi:[1,0,0]
	v_pk_fma_f32 v[106:107], v[106:107], v[106:107], s[22:23] neg_lo:[1,0,0] neg_hi:[1,0,0]
	v_pk_fma_f32 v[108:109], v[108:109], v[108:109], s[22:23] neg_lo:[1,0,0] neg_hi:[1,0,0]
	v_exp_f32_e32 v104, v104
	v_exp_f32_e32 v105, v105
	v_exp_f32_e32 v106, v106
	v_exp_f32_e32 v107, v107
	v_exp_f32_e32 v108, v108
	v_exp_f32_e32 v109, v109
	v_pk_add_f32 v[82:83], v[82:83], v[96:97]
	v_pk_fma_f32 v[86:87], v[96:97], v[46:47], v[86:87]
	v_pk_add_f32 v[90:91], v[90:91], v[98:99]
	v_pk_fma_f32 v[94:95], v[98:99], v[38:39], v[94:95]
	v_pk_add_f32 v[80:81], v[80:81], v[100:101]
	v_pk_fma_f32 v[84:85], v[100:101], v[42:43], v[84:85] op_sel:[0,1,0] op_sel_hi:[1,0,1]
	v_pk_add_f32 v[88:89], v[88:89], v[100:101] op_sel:[0,1] op_sel_hi:[1,0]
	v_pk_fma_f32 v[92:93], v[100:101], v[34:35], v[92:93] op_sel:[1,1,0] op_sel_hi:[0,0,1]
	v_pk_add_f32 v[82:83], v[82:83], v[102:103]
	v_pk_fma_f32 v[86:87], v[102:103], v[44:45], v[86:87] op_sel:[0,1,0] op_sel_hi:[1,0,1]
	v_pk_add_f32 v[90:91], v[90:91], v[102:103] op_sel:[0,1] op_sel_hi:[1,0]
	v_pk_fma_f32 v[94:95], v[102:103], v[36:37], v[94:95] op_sel:[1,1,0] op_sel_hi:[0,0,1]
	v_sub_f32_e32 v96, v42, v25
	v_sub_f32_e32 v98, v41, v26
	v_sub_f32_e32 v100, v44, v27
	v_sub_f32_e32 v102, v43, v28
	v_sub_f32_e32 v97, v46, v29
	v_sub_f32_e32 v99, v45, v30
	v_sub_f32_e32 v101, v42, v33
	v_sub_f32_e32 v103, v41, v34
	v_fma_f32 v96, -v96, v96, s26
	v_fma_f32 v98, -v98, v98, s26
	v_fma_f32 v100, -v100, v100, s26
	v_fma_f32 v102, -v102, v102, s26
	v_fma_f32 v97, -v97, v97, s26
	v_fma_f32 v99, -v99, v99, s26
	v_fma_f32 v101, -v101, v101, s24
	v_fma_f32 v103, -v103, v103, s24
	v_exp_f32_e32 v96, v96
	v_exp_f32_e32 v98, v98
	v_exp_f32_e32 v100, v100
	v_exp_f32_e32 v102, v102
	v_exp_f32_e32 v97, v97
	v_exp_f32_e32 v99, v99
	v_exp_f32_e32 v101, v101
	v_exp_f32_e32 v103, v103
	v_pk_add_f32 v[88:89], v[88:89], v[104:105]
	v_pk_fma_f32 v[92:93], v[104:105], v[40:41], v[92:93]
	v_pk_add_f32 v[90:91], v[90:91], v[106:107]
	v_pk_add_f32 v[88:89], v[88:89], v[106:107]
	v_pk_fma_f32 v[92:93], v[106:107], v[44:45], v[92:93]
	v_pk_fma_f32 v[94:95], v[106:107], v[42:43], v[94:95]
	v_pk_add_f32 v[90:91], v[90:91], v[108:109]
	v_pk_fma_f32 v[94:95], v[108:109], v[46:47], v[94:95]
	v_sub_f32_e32 v108, v44, v35
	v_sub_f32_e32 v110, v43, v36
	v_sub_f32_e32 v105, v46, v37
	v_sub_f32_e32 v107, v45, v38
	v_sub_f32_e32 v109, v42, v41
	v_sub_f32_e32 v104, v43, v42
	v_sub_f32_e32 v111, v44, v43
	v_sub_f32_e32 v106, v45, v44
	v_fma_f32 v108, -v108, v108, s24
	v_fma_f32 v110, -v110, v110, s24
	v_fma_f32 v105, -v105, v105, s24
	v_fma_f32 v107, -v107, v107, s24
	v_fma_f32 v109, -v109, v109, s20
	v_fma_f32 v104, -v104, v104, s20
	v_fma_f32 v111, -v111, v111, s20
	v_fma_f32 v106, -v106, v106, s20
	v_exp_f32_e32 v108, v108
	v_exp_f32_e32 v110, v110
	v_exp_f32_e32 v105, v105
	v_exp_f32_e32 v107, v107
	v_exp_f32_e32 v109, v109
	v_exp_f32_e32 v104, v104
	v_exp_f32_e32 v111, v111
	v_exp_f32_e32 v106, v106
	v_add_f32_e32 v88, v88, v96
	v_fmac_f32_e32 v92, v96, v25
	v_add_f32_e32 v72, v72, v98
	v_fmac_f32_e32 v76, v98, v41
	v_add_f32_e32 v73, v73, v100
	v_fmac_f32_e32 v77, v100, v44
	v_add_f32_e32 v90, v90, v100
	v_fmac_f32_e32 v94, v100, v27
	v_add_f32_e32 v74, v74, v102
	v_fmac_f32_e32 v78, v102, v43
	v_add_f32_e32 v89, v89, v102
	v_fmac_f32_e32 v93, v102, v28
	v_add_f32_e32 v75, v75, v97
	v_fmac_f32_e32 v79, v97, v46
	v_add_f32_e32 v91, v91, v99
	v_fmac_f32_e32 v95, v99, v30
	v_add_f32_e32 v88, v88, v101
	v_fmac_f32_e32 v92, v101, v33
	v_add_f32_e32 v80, v80, v103
	v_fmac_f32_e32 v84, v103, v41
	v_sub_f32_e64 v96, v46, v45
	v_fma_f32 v96, -v96, v96, s20
	s_nop 0
	v_exp_f32_e32 v96, v96
	v_add_f32_e32 v81, v81, v108
	v_fmac_f32_e32 v85, v108, v44
	v_add_f32_e32 v90, v90, v108
	v_fmac_f32_e32 v94, v108, v35
	v_add_f32_e32 v82, v82, v110
	v_fmac_f32_e32 v86, v110, v43
	v_add_f32_e32 v89, v89, v110
	v_fmac_f32_e32 v93, v110, v36
	v_add_f32_e32 v83, v83, v105
	v_fmac_f32_e32 v87, v105, v46
	v_add_f32_e32 v91, v91, v107
	v_fmac_f32_e32 v95, v107, v38
	v_add_f32_e32 v88, v88, v109
	v_fmac_f32_e32 v92, v109, v41
	v_add_f32_e32 v89, v89, v111
	v_fmac_f32_e32 v93, v111, v44
	v_add_f32_e32 v90, v90, v111
	v_fmac_f32_e32 v94, v111, v43
	v_pk_add_f32 v[88:89], v[88:89], v[104:105] op_sel_hi:[1,0]
	v_pk_fma_f32 v[92:93], v[104:105], v[42:43], v[92:93] op_sel:[0,1,0] op_sel_hi:[0,0,1]
	v_pk_add_f32 v[90:91], v[90:91], v[106:107] op_sel_hi:[1,0]
	v_pk_fma_f32 v[94:95], v[106:107], v[44:45], v[94:95] op_sel:[0,1,0] op_sel_hi:[0,0,1]
	s_nop 0
	v_add_f32_e32 v91, v91, v96
	v_fmac_f32_e32 v95, v96, v46
	v_rcp_f32_e32 v96, v72
	v_rcp_f32_e32 v97, v73
	v_rcp_f32_e32 v98, v74
	v_rcp_f32_e64 v99, v75
	v_pk_mul_f32 v[76:77], v[76:77], s[34:35]
	v_pk_mul_f32 v[78:79], v[78:79], s[34:35]
	v_pk_mul_f32 v[76:77], v[76:77], v[96:97]
	v_pk_mul_f32 v[78:79], v[78:79], v[98:99]
	buffer_store_dwordx4 v[76:79], v114, s[12:15], 0 offen offset:2048 sc1
	s_waitcnt vmcnt(5)
	s_nop 0
	v_mov_b32_dpp v48, v52 row_shr:1 row_mask:0xf bank_mask:0xf
	v_mov_b32_dpp v49, v53 row_shr:1 row_mask:0xf bank_mask:0xf
	v_mov_b32_dpp v54, v50 row_shl:1 row_mask:0xf bank_mask:0xf
	v_mov_b32_dpp v55, v51 row_shl:1 row_mask:0xf bank_mask:0xf
	v_pk_mul_f32 v[50:51], v[50:51], s[32:33]
	v_pk_mul_f32 v[52:53], v[52:53], s[32:33]
	v_cndmask_b32_e64 v49, v49, v48, vcc
	v_cndmask_b32_e64 v54, v54, v55, s[16:17]
	v_pk_mul_f32 v[48:49], v[48:49], s[32:33]
	v_pk_mul_f32 v[54:55], v[54:55], s[32:33]
	s_setprio 0
	s_nop 0
	v_pk_add_f32 v[96:97], v[48:49], v[34:35] neg_lo:[0,1] neg_hi:[0,1]
	v_pk_add_f32 v[98:99], v[50:51], v[34:35] neg_lo:[0,1] neg_hi:[0,1]
	v_pk_add_f32 v[100:101], v[52:53], v[34:35] neg_lo:[0,1] neg_hi:[0,1]
	v_pk_add_f32 v[102:103], v[50:51], v[36:37] neg_lo:[0,1] neg_hi:[0,1]
	v_pk_fma_f32 v[96:97], v[96:97], v[96:97], s[28:29] neg_lo:[1,0,0] neg_hi:[1,0,0]
	v_pk_fma_f32 v[98:99], v[98:99], v[98:99], s[22:23] neg_lo:[1,0,0] neg_hi:[1,0,0]
	v_pk_fma_f32 v[100:101], v[100:101], v[100:101], s[28:29] neg_lo:[1,0,0] neg_hi:[1,0,0]
	v_pk_fma_f32 v[102:103], v[102:103], v[102:103], s[28:29] neg_lo:[1,0,0] neg_hi:[1,0,0]
	v_exp_f32_e32 v96, v96
	v_exp_f32_e32 v97, v97
	v_exp_f32_e32 v98, v98
	v_exp_f32_e32 v99, v99
	v_exp_f32_e32 v100, v100
	v_exp_f32_e32 v101, v101
	v_exp_f32_e32 v102, v102
	v_exp_f32_e32 v103, v103
	v_pk_add_f32 v[104:105], v[52:53], v[36:37] neg_lo:[0,1] neg_hi:[0,1]
	v_pk_add_f32 v[106:107], v[54:55], v[36:37] neg_lo:[0,1] neg_hi:[0,1]
	v_pk_add_f32 v[108:109], v[50:51], v[34:35] op_sel:[1,0] op_sel_hi:[0,1] neg_lo:[0,1] neg_hi:[0,1]
	v_pk_add_f32 v[110:111], v[52:53], v[36:37] op_sel:[1,0] op_sel_hi:[0,1] neg_lo:[0,1] neg_hi:[0,1]
	v_pk_fma_f32 v[104:105], v[104:105], v[104:105], s[22:23] neg_lo:[1,0,0] neg_hi:[1,0,0]
	v_pk_fma_f32 v[106:107], v[106:107], v[106:107], s[28:29] neg_lo:[1,0,0] neg_hi:[1,0,0]
	v_pk_fma_f32 v[108:109], v[108:109], v[108:109], s[26:27] neg_lo:[1,0,0] neg_hi:[1,0,0]
	v_pk_fma_f32 v[110:111], v[110:111], v[110:111], s[26:27] neg_lo:[1,0,0] neg_hi:[1,0,0]
	v_exp_f32_e32 v104, v104
	v_exp_f32_e32 v105, v105
	v_exp_f32_e32 v106, v106
	v_exp_f32_e32 v107, v107
	v_exp_f32_e32 v108, v108
	v_exp_f32_e32 v109, v109
	v_exp_f32_e32 v110, v110
	v_exp_f32_e32 v111, v111
	v_pk_add_f32 v[80:81], v[80:81], v[96:97]
	v_pk_fma_f32 v[84:85], v[96:97], v[48:49], v[84:85]
	v_pk_add_f32 v[82:83], v[82:83], v[102:103]
	v_pk_add_f32 v[80:81], v[80:81], v[98:99]
	v_pk_fma_f32 v[84:85], v[98:99], v[50:51], v[84:85]
	v_pk_fma_f32 v[86:87], v[102:103], v[50:51], v[86:87]
	v_pk_add_f32 v[80:81], v[80:81], v[100:101]
	v_pk_fma_f32 v[84:85], v[100:101], v[52:53], v[84:85]
	v_pk_add_f32 v[96:97], v[48:49], v[42:43] neg_lo:[0,1] neg_hi:[0,1]
	v_pk_add_f32 v[98:99], v[50:51], v[42:43] neg_lo:[0,1] neg_hi:[0,1]
	v_pk_add_f32 v[100:101], v[52:53], v[42:43] neg_lo:[0,1] neg_hi:[0,1]
	v_pk_add_f32 v[102:103], v[50:51], v[44:45] neg_lo:[0,1] neg_hi:[0,1]
	v_pk_fma_f32 v[96:97], v[96:97], v[96:97], s[26:27] neg_lo:[1,0,0] neg_hi:[1,0,0]
	v_pk_fma_f32 v[98:99], v[98:99], v[98:99], s[20:21] neg_lo:[1,0,0] neg_hi:[1,0,0]
	v_pk_fma_f32 v[100:101], v[100:101], v[100:101], s[26:27] neg_lo:[1,0,0] neg_hi:[1,0,0]
	v_pk_fma_f32 v[102:103], v[102:103], v[102:103], s[26:27] neg_lo:[1,0,0] neg_hi:[1,0,0]
	v_exp_f32_e32 v96, v96
	v_exp_f32_e32 v97, v97
	v_exp_f32_e32 v98, v98
	v_exp_f32_e32 v99, v99
	v_exp_f32_e32 v100, v100
	v_exp_f32_e32 v101, v101
	v_exp_f32_e32 v102, v102
	v_exp_f32_e32 v103, v103
	v_pk_add_f32 v[82:83], v[82:83], v[104:105]
	v_pk_fma_f32 v[86:87], v[104:105], v[52:53], v[86:87]
	v_pk_add_f32 v[80:81], v[80:81], v[108:109]
	v_pk_add_f32 v[82:83], v[82:83], v[106:107]
	v_pk_fma_f32 v[86:87], v[106:107], v[54:55], v[86:87]
	v_pk_fma_f32 v[84:85], v[108:109], v[50:51], v[84:85] op_sel:[0,1,0] op_sel_hi:[1,0,1]
	v_pk_add_f32 v[82:83], v[82:83], v[110:111]
	v_pk_fma_f32 v[86:87], v[110:111], v[52:53], v[86:87] op_sel:[0,1,0] op_sel_hi:[1,0,1]
	v_pk_add_f32 v[104:105], v[52:53], v[44:45] neg_lo:[0,1] neg_hi:[0,1]
	v_pk_add_f32 v[106:107], v[54:55], v[44:45] neg_lo:[0,1] neg_hi:[0,1]
	v_pk_add_f32 v[108:109], v[50:51], v[42:43] op_sel:[1,0] op_sel_hi:[0,1] neg_lo:[0,1] neg_hi:[0,1]
	v_pk_add_f32 v[110:111], v[52:53], v[44:45] op_sel:[1,0] op_sel_hi:[0,1] neg_lo:[0,1] neg_hi:[0,1]
	v_pk_fma_f32 v[104:105], v[104:105], v[104:105], s[20:21] neg_lo:[1,0,0] neg_hi:[1,0,0]
	v_pk_fma_f32 v[106:107], v[106:107], v[106:107], s[26:27] neg_lo:[1,0,0] neg_hi:[1,0,0]
	v_pk_fma_f32 v[108:109], v[108:109], v[108:109], s[24:25] neg_lo:[1,0,0] neg_hi:[1,0,0]
	v_pk_fma_f32 v[110:111], v[110:111], v[110:111], s[24:25] neg_lo:[1,0,0] neg_hi:[1,0,0]
	v_exp_f32_e32 v104, v104
	v_exp_f32_e32 v105, v105
	v_exp_f32_e32 v106, v106
	v_exp_f32_e32 v107, v107
	v_exp_f32_e32 v108, v108
	v_exp_f32_e32 v109, v109
	v_exp_f32_e32 v110, v110
	v_exp_f32_e32 v111, v111
	v_pk_add_f32 v[88:89], v[88:89], v[96:97]
	v_pk_fma_f32 v[92:93], v[96:97], v[48:49], v[92:93]
	v_pk_add_f32 v[90:91], v[90:91], v[102:103]
	v_pk_add_f32 v[88:89], v[88:89], v[98:99]
	v_pk_fma_f32 v[92:93], v[98:99], v[50:51], v[92:93]
	v_pk_fma_f32 v[94:95], v[102:103], v[50:51], v[94:95]
	v_pk_add_f32 v[88:89], v[88:89], v[100:101]
	v_pk_fma_f32 v[92:93], v[100:101], v[52:53], v[92:93]
	v_sub_f32_e32 v96, v49, v34
	v_sub_f32_e32 v98, v52, v35
	v_sub_f32_e32 v100, v51, v36
	v_sub_f32_e32 v102, v54, v37
	v_sub_f32_e32 v97, v49, v42
	v_sub_f32_e32 v99, v52, v43
	v_sub_f32_e32 v101, v51, v44
	v_sub_f32_e32 v103, v54, v45
	v_fma_f32 v96, -v96, v96, s26
	v_fma_f32 v98, -v98, v98, s26
	v_fma_f32 v100, -v100, v100, s26
	v_fma_f32 v102, -v102, v102, s26
	v_fma_f32 v97, -v97, v97, s24
	v_fma_f32 v99, -v99, v99, s24
	v_fma_f32 v101, -v101, v101, s24
	v_fma_f32 v103, -v103, v103, s24
	v_exp_f32_e32 v96, v96
	v_exp_f32_e32 v98, v98
	v_exp_f32_e32 v100, v100
	v_exp_f32_e32 v102, v102
	v_exp_f32_e32 v97, v97
	v_exp_f32_e32 v99, v99
	v_exp_f32_e32 v101, v101
	v_exp_f32_e32 v103, v103
	v_pk_add_f32 v[90:91], v[90:91], v[104:105]
	v_pk_fma_f32 v[94:95], v[104:105], v[52:53], v[94:95]
	v_pk_add_f32 v[88:89], v[88:89], v[108:109]
	v_pk_add_f32 v[90:91], v[90:91], v[106:107]
	v_pk_fma_f32 v[94:95], v[106:107], v[54:55], v[94:95]
	v_pk_fma_f32 v[92:93], v[108:109], v[50:51], v[92:93] op_sel:[0,1,0] op_sel_hi:[1,0,1]
	v_pk_add_f32 v[90:91], v[90:91], v[110:111]
	v_pk_fma_f32 v[94:95], v[110:111], v[52:53], v[94:95] op_sel:[0,1,0] op_sel_hi:[1,0,1]
	v_add_f32_e32 v80, v80, v96
	v_fmac_f32_e32 v84, v96, v49
	v_add_f32_e32 v81, v81, v98
	v_fmac_f32_e32 v85, v98, v52
	v_add_f32_e32 v82, v82, v100
	v_fmac_f32_e32 v86, v100, v51
	v_add_f32_e32 v83, v83, v102
	v_fmac_f32_e32 v87, v102, v54
	v_add_f32_e32 v88, v88, v97
	v_fmac_f32_e32 v92, v97, v49
	v_add_f32_e32 v89, v89, v99
	v_fmac_f32_e32 v93, v99, v52
	v_add_f32_e32 v90, v90, v101
	v_fmac_f32_e32 v94, v101, v51
	v_add_f32_e32 v91, v91, v103
	v_fmac_f32_e32 v95, v103, v54
	v_rcp_f32_e32 v96, v80
	v_rcp_f32_e32 v97, v81
	v_rcp_f32_e32 v98, v82
	v_rcp_f32_e32 v99, v83
	v_pk_mul_f32 v[84:85], v[84:85], s[34:35]
	v_pk_mul_f32 v[86:87], v[86:87], s[34:35]
	v_pk_mul_f32 v[84:85], v[84:85], v[96:97]
	v_pk_mul_f32 v[86:87], v[86:87], v[98:99]
	buffer_store_dwordx4 v[84:87], v119, s[12:15], 0 offen sc1
	s_waitcnt vmcnt(3)
	s_nop 0
	v_mov_b32_dpp v56, v60 row_shr:1 row_mask:0xf bank_mask:0xf
	v_mov_b32_dpp v57, v61 row_shr:1 row_mask:0xf bank_mask:0xf
	v_mov_b32_dpp v62, v58 row_shl:1 row_mask:0xf bank_mask:0xf
	v_mov_b32_dpp v63, v59 row_shl:1 row_mask:0xf bank_mask:0xf
	v_pk_mul_f32 v[58:59], v[58:59], s[32:33]
	v_pk_mul_f32 v[60:61], v[60:61], s[32:33]
	v_cndmask_b32_e64 v57, v57, v56, vcc
	v_cndmask_b32_e64 v62, v62, v63, s[16:17]
	v_pk_mul_f32 v[56:57], v[56:57], s[32:33]
	v_pk_mul_f32 v[62:63], v[62:63], s[32:33]
	s_setprio 0
	s_nop 0
	v_pk_add_f32 v[96:97], v[56:57], v[42:43] neg_lo:[0,1] neg_hi:[0,1]
	v_pk_add_f32 v[98:99], v[58:59], v[42:43] neg_lo:[0,1] neg_hi:[0,1]
	v_pk_add_f32 v[100:101], v[60:61], v[42:43] neg_lo:[0,1] neg_hi:[0,1]
	v_pk_add_f32 v[102:103], v[58:59], v[44:45] neg_lo:[0,1] neg_hi:[0,1]
	v_pk_fma_f32 v[96:97], v[96:97], v[96:97], s[28:29] neg_lo:[1,0,0] neg_hi:[1,0,0]
	v_pk_fma_f32 v[98:99], v[98:99], v[98:99], s[22:23] neg_lo:[1,0,0] neg_hi:[1,0,0]
	v_pk_fma_f32 v[100:101], v[100:101], v[100:101], s[28:29] neg_lo:[1,0,0] neg_hi:[1,0,0]
	v_pk_fma_f32 v[102:103], v[102:103], v[102:103], s[28:29] neg_lo:[1,0,0] neg_hi:[1,0,0]
	v_exp_f32_e32 v96, v96
	v_exp_f32_e32 v97, v97
	v_exp_f32_e32 v98, v98
	v_exp_f32_e32 v99, v99
	v_exp_f32_e32 v100, v100
	v_exp_f32_e32 v101, v101
	v_exp_f32_e32 v102, v102
	v_exp_f32_e32 v103, v103
	v_pk_add_f32 v[104:105], v[60:61], v[44:45] neg_lo:[0,1] neg_hi:[0,1]
	v_pk_add_f32 v[106:107], v[62:63], v[44:45] neg_lo:[0,1] neg_hi:[0,1]
	v_pk_add_f32 v[108:109], v[58:59], v[42:43] op_sel:[1,0] op_sel_hi:[0,1] neg_lo:[0,1] neg_hi:[0,1]
	v_pk_add_f32 v[110:111], v[60:61], v[44:45] op_sel:[1,0] op_sel_hi:[0,1] neg_lo:[0,1] neg_hi:[0,1]
	v_pk_fma_f32 v[104:105], v[104:105], v[104:105], s[22:23] neg_lo:[1,0,0] neg_hi:[1,0,0]
	v_pk_fma_f32 v[106:107], v[106:107], v[106:107], s[28:29] neg_lo:[1,0,0] neg_hi:[1,0,0]
	v_pk_fma_f32 v[108:109], v[108:109], v[108:109], s[26:27] neg_lo:[1,0,0] neg_hi:[1,0,0]
	v_pk_fma_f32 v[110:111], v[110:111], v[110:111], s[26:27] neg_lo:[1,0,0] neg_hi:[1,0,0]
	v_exp_f32_e32 v104, v104
	v_exp_f32_e32 v105, v105
	v_exp_f32_e32 v106, v106
	v_exp_f32_e32 v107, v107
	v_exp_f32_e32 v108, v108
	v_exp_f32_e32 v109, v109
	v_exp_f32_e32 v110, v110
	v_exp_f32_e32 v111, v111
	v_pk_add_f32 v[88:89], v[88:89], v[96:97]
	v_pk_fma_f32 v[92:93], v[96:97], v[56:57], v[92:93]
	v_pk_add_f32 v[90:91], v[90:91], v[102:103]
	v_pk_add_f32 v[88:89], v[88:89], v[98:99]
	v_pk_fma_f32 v[92:93], v[98:99], v[58:59], v[92:93]
	v_pk_fma_f32 v[94:95], v[102:103], v[58:59], v[94:95]
	v_pk_add_f32 v[88:89], v[88:89], v[100:101]
	v_pk_fma_f32 v[92:93], v[100:101], v[60:61], v[92:93]
	v_sub_f32_e32 v96, v57, v42
	v_sub_f32_e32 v98, v60, v43
	v_sub_f32_e32 v100, v59, v44
	v_sub_f32_e32 v102, v62, v45
	v_fma_f32 v96, -v96, v96, s26
	v_fma_f32 v98, -v98, v98, s26
	v_fma_f32 v100, -v100, v100, s26
	v_fma_f32 v102, -v102, v102, s26
	v_exp_f32_e32 v96, v96
	v_exp_f32_e32 v98, v98
	v_exp_f32_e32 v100, v100
	v_exp_f32_e32 v102, v102
	v_pk_add_f32 v[90:91], v[90:91], v[104:105]
	v_pk_fma_f32 v[94:95], v[104:105], v[60:61], v[94:95]
	v_pk_add_f32 v[88:89], v[88:89], v[108:109]
	v_pk_add_f32 v[90:91], v[90:91], v[106:107]
	v_pk_fma_f32 v[94:95], v[106:107], v[62:63], v[94:95]
	v_pk_fma_f32 v[92:93], v[108:109], v[58:59], v[92:93] op_sel:[0,1,0] op_sel_hi:[1,0,1]
	v_pk_add_f32 v[90:91], v[90:91], v[110:111]
	v_pk_fma_f32 v[94:95], v[110:111], v[60:61], v[94:95] op_sel:[0,1,0] op_sel_hi:[1,0,1]
	v_add_f32_e32 v88, v88, v96
	v_fmac_f32_e32 v92, v96, v57
	v_add_f32_e32 v89, v89, v98
	v_fmac_f32_e32 v93, v98, v60
	v_add_f32_e32 v90, v90, v100
	v_fmac_f32_e32 v94, v100, v59
	v_add_f32_e32 v91, v91, v102
	v_fmac_f32_e32 v95, v102, v62
	v_rcp_f32_e32 v96, v88
	v_rcp_f32_e32 v97, v89
	v_rcp_f32_e32 v98, v90
	v_rcp_f32_e32 v99, v91
	v_pk_mul_f32 v[92:93], v[92:93], s[34:35]
	v_pk_mul_f32 v[94:95], v[94:95], s[34:35]
	v_pk_mul_f32 v[92:93], v[92:93], v[96:97]
	v_pk_mul_f32 v[94:95], v[94:95], v[98:99]
	buffer_store_dwordx4 v[92:95], v119, s[12:15], 0 offen offset:2048 sc1
	s_endpgm
